# merge epilogue: seven of sixteen positions of next-branch gates carried in spare VGPRs (v168-171 added)
# speedup vs baseline: 1.0148x; 1.0023x over previous
.LBB0_1217:
	s_ashr_i32 s30, s63, 2
	s_lshl_b32 s4, s30, 15
	s_lshl_b32 s5, s67, 8
	s_sub_i32 s4, s5, s4
	v_add_u32_e32 v2, s4, v165
	s_lshl_b32 s5, s63, 8
	s_and_b32 s5, s5, 0x300
	v_add_u32_e32 v0, s5, v189
	v_mul_u32_u24_e32 v191, 0x1800, v2
	v_lshl_add_u32 v191, v0, 1, v191
	v_lshlrev_b32_e32 v3, 11, v2
	v_lshl_add_u32 v3, v0, 1, v3
	v_bfe_u32 v2, v165, 6, 1
	v_lshlrev_b32_e32 v2, 12, v2
	v_bfe_u32 v0, v189, 5, 2
	v_lshl_add_u32 v2, v0, 10, v2
	v_bfe_u32 v0, v189, 3, 2
	v_lshl_add_u32 v2, v0, 8, v2
	v_and_b32_e32 v0, 15, v165
	v_lshl_add_u32 v2, v0, 4, v2
	v_add_u32_e32 v2, 0x21000, v2
	s_lshl_b32 s26, s30, 11
	s_add_u32 s26, s14, s26
	s_addc_u32 s27, s15, 0
	s_cmp_eq_u32 s30, 2
	s_cbranch_scc1 .Lmg_last
	s_cmp_eq_u32 s30, 1
	s_cbranch_scc1 .Lmg_mid
	s_add_u32 s28, s26, 0x0
	s_addc_u32 s29, s27, 0
	global_load_dwordx4 v[132:135], v191, s[28:29]
	global_load_dwordx4 v[136:139], v191, s[28:29] offset:2048
	s_add_u32 s28, s26, 0x0
	s_addc_u32 s29, s27, 0
	global_load_dwordx4 v[140:143], v191, s[28:29] offset:256
	global_load_dwordx4 v[144:147], v191, s[28:29] offset:2304
	s_add_u32 s28, s26, 0x18000
	s_addc_u32 s29, s27, 0
	global_load_dwordx4 v[148:151], v191, s[28:29]
	global_load_dwordx4 v[152:155], v191, s[28:29] offset:2048
	s_add_u32 s28, s26, 0x18000
	s_addc_u32 s29, s27, 0
	global_load_dwordx4 v[156:159], v191, s[28:29] offset:256
	global_load_dwordx4 v[160:163], v191, s[28:29] offset:2304
	s_add_u32 s28, s26, 0x30000
	s_addc_u32 s29, s27, 0
	global_load_dwordx4 v[180:183], v191, s[28:29]
	global_load_dwordx4 v[184:187], v191, s[28:29] offset:2048
	s_add_u32 s28, s26, 0x30000
	s_addc_u32 s29, s27, 0
	global_load_dwordx4 v[192:195], v191, s[28:29] offset:256
	global_load_dwordx4 v[196:199], v191, s[28:29] offset:2304
	s_add_u32 s28, s26, 0x48000
	s_addc_u32 s29, s27, 0
	global_load_dwordx4 v[212:215], v191, s[28:29]
	global_load_dwordx4 v[216:219], v191, s[28:29] offset:2048
	s_and_b64 vcc, exec, s[20:21]
	s_cbranch_vccz .Lmg_nba
	s_barrier
.Lmg_nba:
	s_waitcnt vmcnt(12)
	v_lshlrev_b32_e32 v220, 16, v132
	v_and_b32_e32 v221, 0xffff0000, v132
	v_lshlrev_b32_e32 v222, 16, v133
	v_and_b32_e32 v223, 0xffff0000, v133
	v_lshlrev_b32_e32 v224, 16, v134
	v_and_b32_e32 v225, 0xffff0000, v134
	v_lshlrev_b32_e32 v226, 16, v135
	v_and_b32_e32 v227, 0xffff0000, v135
	v_max_f32_e32 v220, 0x1e3ce508, v220
	v_max_f32_e32 v221, 0x1e3ce508, v221
	v_max_f32_e32 v222, 0x1e3ce508, v222
	v_max_f32_e32 v223, 0x1e3ce508, v223
	v_max_f32_e32 v224, 0x1e3ce508, v224
	v_max_f32_e32 v225, 0x1e3ce508, v225
	v_max_f32_e32 v226, 0x1e3ce508, v226
	v_max_f32_e32 v227, 0x1e3ce508, v227
	v_mov_b32_e32 v228, v136
	v_mov_b32_e32 v229, v137
	v_mov_b32_e32 v230, v138
	v_mov_b32_e32 v231, v139
	v_lshlrev_b32_e32 v132, 16, v136
	v_and_b32_e32 v133, 0xffff0000, v136
	v_lshlrev_b32_e32 v134, 16, v137
	v_and_b32_e32 v135, 0xffff0000, v137
	v_lshlrev_b32_e32 v136, 16, v138
	v_and_b32_e32 v137, 0xffff0000, v138
	v_lshlrev_b32_e32 v138, 16, v139
	v_and_b32_e32 v139, 0xffff0000, v139
	v_max_f32_e32 v132, 0x1e3ce508, v132
	v_max_f32_e32 v133, 0x1e3ce508, v133
	v_max_f32_e32 v134, 0x1e3ce508, v134
	v_max_f32_e32 v135, 0x1e3ce508, v135
	v_max_f32_e32 v136, 0x1e3ce508, v136
	v_max_f32_e32 v137, 0x1e3ce508, v137
	v_max_f32_e32 v138, 0x1e3ce508, v138
	v_max_f32_e32 v139, 0x1e3ce508, v139
	v_rcp_f32_e32 v132, v132
	v_rcp_f32_e32 v133, v133
	v_rcp_f32_e32 v134, v134
	v_rcp_f32_e32 v135, v135
	v_rcp_f32_e32 v136, v136
	v_rcp_f32_e32 v137, v137
	v_rcp_f32_e32 v138, v138
	v_rcp_f32_e32 v139, v139
	v_pk_mul_f32 v[220:221], v[220:221], v[132:133]
	v_pk_mul_f32 v[222:223], v[222:223], v[134:135]
	v_pk_mul_f32 v[224:225], v[224:225], v[136:137]
	v_pk_mul_f32 v[226:227], v[226:227], v[138:139]
	v_pk_mul_f32 v[112:113], v[112:113], v[220:221]
	v_pk_mul_f32 v[114:115], v[114:115], v[222:223]
	v_pk_mul_f32 v[108:109], v[108:109], v[224:225]
	v_pk_mul_f32 v[110:111], v[110:111], v[226:227]
	s_add_u32 s28, s26, 0x48000
	s_addc_u32 s29, s27, 0
	global_load_dwordx4 v[132:135], v191, s[28:29] offset:256
	global_load_dwordx4 v[136:139], v191, s[28:29] offset:2304
	s_waitcnt vmcnt(12)
	v_lshlrev_b32_e32 v220, 16, v140
	v_and_b32_e32 v221, 0xffff0000, v140
	v_lshlrev_b32_e32 v222, 16, v141
	v_and_b32_e32 v223, 0xffff0000, v141
	v_lshlrev_b32_e32 v224, 16, v142
	v_and_b32_e32 v225, 0xffff0000, v142
	v_lshlrev_b32_e32 v226, 16, v143
	v_and_b32_e32 v227, 0xffff0000, v143
	v_max_f32_e32 v220, 0x1e3ce508, v220
	v_max_f32_e32 v221, 0x1e3ce508, v221
	v_max_f32_e32 v222, 0x1e3ce508, v222
	v_max_f32_e32 v223, 0x1e3ce508, v223
	v_max_f32_e32 v224, 0x1e3ce508, v224
	v_max_f32_e32 v225, 0x1e3ce508, v225
	v_max_f32_e32 v226, 0x1e3ce508, v226
	v_max_f32_e32 v227, 0x1e3ce508, v227
	v_mov_b32_e32 v232, v144
	v_mov_b32_e32 v233, v145
	v_mov_b32_e32 v234, v146
	v_mov_b32_e32 v235, v147
	v_lshlrev_b32_e32 v140, 16, v144
	v_and_b32_e32 v141, 0xffff0000, v144
	v_lshlrev_b32_e32 v142, 16, v145
	v_and_b32_e32 v143, 0xffff0000, v145
	v_lshlrev_b32_e32 v144, 16, v146
	v_and_b32_e32 v145, 0xffff0000, v146
	v_lshlrev_b32_e32 v146, 16, v147
	v_and_b32_e32 v147, 0xffff0000, v147
	v_max_f32_e32 v140, 0x1e3ce508, v140
	v_max_f32_e32 v141, 0x1e3ce508, v141
	v_max_f32_e32 v142, 0x1e3ce508, v142
	v_max_f32_e32 v143, 0x1e3ce508, v143
	v_max_f32_e32 v144, 0x1e3ce508, v144
	v_max_f32_e32 v145, 0x1e3ce508, v145
	v_max_f32_e32 v146, 0x1e3ce508, v146
	v_max_f32_e32 v147, 0x1e3ce508, v147
	v_rcp_f32_e32 v140, v140
	v_rcp_f32_e32 v141, v141
	v_rcp_f32_e32 v142, v142
	v_rcp_f32_e32 v143, v143
	v_rcp_f32_e32 v144, v144
	v_rcp_f32_e32 v145, v145
	v_rcp_f32_e32 v146, v146
	v_rcp_f32_e32 v147, v147
	v_pk_mul_f32 v[220:221], v[220:221], v[140:141]
	v_pk_mul_f32 v[222:223], v[222:223], v[142:143]
	v_pk_mul_f32 v[224:225], v[224:225], v[144:145]
	v_pk_mul_f32 v[226:227], v[226:227], v[146:147]
	v_pk_mul_f32 v[80:81], v[80:81], v[220:221]
	v_pk_mul_f32 v[82:83], v[82:83], v[222:223]
	v_pk_mul_f32 v[76:77], v[76:77], v[224:225]
	v_pk_mul_f32 v[78:79], v[78:79], v[226:227]
	s_add_u32 s28, s26, 0xc0000
	s_addc_u32 s29, s27, 0
	global_load_dwordx4 v[140:143], v191, s[28:29]
	global_load_dwordx4 v[144:147], v191, s[28:29] offset:2048
	s_waitcnt vmcnt(12)
	v_lshlrev_b32_e32 v220, 16, v148
	v_and_b32_e32 v221, 0xffff0000, v148
	v_lshlrev_b32_e32 v222, 16, v149
	v_and_b32_e32 v223, 0xffff0000, v149
	v_lshlrev_b32_e32 v224, 16, v150
	v_and_b32_e32 v225, 0xffff0000, v150
	v_lshlrev_b32_e32 v226, 16, v151
	v_and_b32_e32 v227, 0xffff0000, v151
	v_max_f32_e32 v220, 0x1e3ce508, v220
	v_max_f32_e32 v221, 0x1e3ce508, v221
	v_max_f32_e32 v222, 0x1e3ce508, v222
	v_max_f32_e32 v223, 0x1e3ce508, v223
	v_max_f32_e32 v224, 0x1e3ce508, v224
	v_max_f32_e32 v225, 0x1e3ce508, v225
	v_max_f32_e32 v226, 0x1e3ce508, v226
	v_max_f32_e32 v227, 0x1e3ce508, v227
	v_mov_b32_e32 v236, v152
	v_mov_b32_e32 v237, v153
	v_mov_b32_e32 v238, v154
	v_mov_b32_e32 v239, v155
	v_lshlrev_b32_e32 v148, 16, v152
	v_and_b32_e32 v149, 0xffff0000, v152
	v_lshlrev_b32_e32 v150, 16, v153
	v_and_b32_e32 v151, 0xffff0000, v153
	v_lshlrev_b32_e32 v152, 16, v154
	v_and_b32_e32 v153, 0xffff0000, v154
	v_lshlrev_b32_e32 v154, 16, v155
	v_and_b32_e32 v155, 0xffff0000, v155
	v_max_f32_e32 v148, 0x1e3ce508, v148
	v_max_f32_e32 v149, 0x1e3ce508, v149
	v_max_f32_e32 v150, 0x1e3ce508, v150
	v_max_f32_e32 v151, 0x1e3ce508, v151
	v_max_f32_e32 v152, 0x1e3ce508, v152
	v_max_f32_e32 v153, 0x1e3ce508, v153
	v_max_f32_e32 v154, 0x1e3ce508, v154
	v_max_f32_e32 v155, 0x1e3ce508, v155
	v_rcp_f32_e32 v148, v148
	v_rcp_f32_e32 v149, v149
	v_rcp_f32_e32 v150, v150
	v_rcp_f32_e32 v151, v151
	v_rcp_f32_e32 v152, v152
	v_rcp_f32_e32 v153, v153
	v_rcp_f32_e32 v154, v154
	v_rcp_f32_e32 v155, v155
	v_pk_mul_f32 v[220:221], v[220:221], v[148:149]
	v_pk_mul_f32 v[222:223], v[222:223], v[150:151]
	v_pk_mul_f32 v[224:225], v[224:225], v[152:153]
	v_pk_mul_f32 v[226:227], v[226:227], v[154:155]
	v_pk_mul_f32 v[104:105], v[104:105], v[220:221]
	v_pk_mul_f32 v[106:107], v[106:107], v[222:223]
	v_pk_mul_f32 v[100:101], v[100:101], v[224:225]
	v_pk_mul_f32 v[102:103], v[102:103], v[226:227]
	s_add_u32 s28, s26, 0xc0000
	s_addc_u32 s29, s27, 0
	global_load_dwordx4 v[148:151], v191, s[28:29] offset:256
	global_load_dwordx4 v[152:155], v191, s[28:29] offset:2304
	s_waitcnt vmcnt(12)
	v_lshlrev_b32_e32 v220, 16, v156
	v_and_b32_e32 v221, 0xffff0000, v156
	v_lshlrev_b32_e32 v222, 16, v157
	v_and_b32_e32 v223, 0xffff0000, v157
	v_lshlrev_b32_e32 v224, 16, v158
	v_and_b32_e32 v225, 0xffff0000, v158
	v_lshlrev_b32_e32 v226, 16, v159
	v_and_b32_e32 v227, 0xffff0000, v159
	v_max_f32_e32 v220, 0x1e3ce508, v220
	v_max_f32_e32 v221, 0x1e3ce508, v221
	v_max_f32_e32 v222, 0x1e3ce508, v222
	v_max_f32_e32 v223, 0x1e3ce508, v223
	v_max_f32_e32 v224, 0x1e3ce508, v224
	v_max_f32_e32 v225, 0x1e3ce508, v225
	v_max_f32_e32 v226, 0x1e3ce508, v226
	v_max_f32_e32 v227, 0x1e3ce508, v227
	v_mov_b32_e32 v240, v160
	v_mov_b32_e32 v241, v161
	v_mov_b32_e32 v242, v162
	v_mov_b32_e32 v243, v163
	v_lshlrev_b32_e32 v156, 16, v160
	v_and_b32_e32 v157, 0xffff0000, v160
	v_lshlrev_b32_e32 v158, 16, v161
	v_and_b32_e32 v159, 0xffff0000, v161
	v_lshlrev_b32_e32 v160, 16, v162
	v_and_b32_e32 v161, 0xffff0000, v162
	v_lshlrev_b32_e32 v162, 16, v163
	v_and_b32_e32 v163, 0xffff0000, v163
	v_max_f32_e32 v156, 0x1e3ce508, v156
	v_max_f32_e32 v157, 0x1e3ce508, v157
	v_max_f32_e32 v158, 0x1e3ce508, v158
	v_max_f32_e32 v159, 0x1e3ce508, v159
	v_max_f32_e32 v160, 0x1e3ce508, v160
	v_max_f32_e32 v161, 0x1e3ce508, v161
	v_max_f32_e32 v162, 0x1e3ce508, v162
	v_max_f32_e32 v163, 0x1e3ce508, v163
	v_rcp_f32_e32 v156, v156
	v_rcp_f32_e32 v157, v157
	v_rcp_f32_e32 v158, v158
	v_rcp_f32_e32 v159, v159
	v_rcp_f32_e32 v160, v160
	v_rcp_f32_e32 v161, v161
	v_rcp_f32_e32 v162, v162
	v_rcp_f32_e32 v163, v163
	v_pk_mul_f32 v[220:221], v[220:221], v[156:157]
	v_pk_mul_f32 v[222:223], v[222:223], v[158:159]
	v_pk_mul_f32 v[224:225], v[224:225], v[160:161]
	v_pk_mul_f32 v[226:227], v[226:227], v[162:163]
	v_pk_mul_f32 v[72:73], v[72:73], v[220:221]
	v_pk_mul_f32 v[74:75], v[74:75], v[222:223]
	v_pk_mul_f32 v[68:69], v[68:69], v[224:225]
	v_pk_mul_f32 v[70:71], v[70:71], v[226:227]
	s_add_u32 s28, s26, 0xd8000
	s_addc_u32 s29, s27, 0
	global_load_dwordx4 v[156:159], v191, s[28:29]
	global_load_dwordx4 v[160:163], v191, s[28:29] offset:2048
	s_waitcnt vmcnt(12)
	v_lshlrev_b32_e32 v220, 16, v180
	v_and_b32_e32 v221, 0xffff0000, v180
	v_lshlrev_b32_e32 v222, 16, v181
	v_and_b32_e32 v223, 0xffff0000, v181
	v_lshlrev_b32_e32 v224, 16, v182
	v_and_b32_e32 v225, 0xffff0000, v182
	v_lshlrev_b32_e32 v226, 16, v183
	v_and_b32_e32 v227, 0xffff0000, v183
	v_max_f32_e32 v220, 0x1e3ce508, v220
	v_max_f32_e32 v221, 0x1e3ce508, v221
	v_max_f32_e32 v222, 0x1e3ce508, v222
	v_max_f32_e32 v223, 0x1e3ce508, v223
	v_max_f32_e32 v224, 0x1e3ce508, v224
	v_max_f32_e32 v225, 0x1e3ce508, v225
	v_max_f32_e32 v226, 0x1e3ce508, v226
	v_max_f32_e32 v227, 0x1e3ce508, v227
	v_mov_b32_e32 v244, v184
	v_mov_b32_e32 v245, v185
	v_mov_b32_e32 v246, v186
	v_mov_b32_e32 v247, v187
	v_lshlrev_b32_e32 v180, 16, v184
	v_and_b32_e32 v181, 0xffff0000, v184
	v_lshlrev_b32_e32 v182, 16, v185
	v_and_b32_e32 v183, 0xffff0000, v185
	v_lshlrev_b32_e32 v184, 16, v186
	v_and_b32_e32 v185, 0xffff0000, v186
	v_lshlrev_b32_e32 v186, 16, v187
	v_and_b32_e32 v187, 0xffff0000, v187
	v_max_f32_e32 v180, 0x1e3ce508, v180
	v_max_f32_e32 v181, 0x1e3ce508, v181
	v_max_f32_e32 v182, 0x1e3ce508, v182
	v_max_f32_e32 v183, 0x1e3ce508, v183
	v_max_f32_e32 v184, 0x1e3ce508, v184
	v_max_f32_e32 v185, 0x1e3ce508, v185
	v_max_f32_e32 v186, 0x1e3ce508, v186
	v_max_f32_e32 v187, 0x1e3ce508, v187
	v_rcp_f32_e32 v180, v180
	v_rcp_f32_e32 v181, v181
	v_rcp_f32_e32 v182, v182
	v_rcp_f32_e32 v183, v183
	v_rcp_f32_e32 v184, v184
	v_rcp_f32_e32 v185, v185
	v_rcp_f32_e32 v186, v186
	v_rcp_f32_e32 v187, v187
	v_pk_mul_f32 v[220:221], v[220:221], v[180:181]
	v_pk_mul_f32 v[222:223], v[222:223], v[182:183]
	v_pk_mul_f32 v[224:225], v[224:225], v[184:185]
	v_pk_mul_f32 v[226:227], v[226:227], v[186:187]
	v_pk_mul_f32 v[96:97], v[96:97], v[220:221]
	v_pk_mul_f32 v[98:99], v[98:99], v[222:223]
	v_pk_mul_f32 v[92:93], v[92:93], v[224:225]
	v_pk_mul_f32 v[94:95], v[94:95], v[226:227]
	s_add_u32 s28, s26, 0xd8000
	s_addc_u32 s29, s27, 0
	global_load_dwordx4 v[180:183], v191, s[28:29] offset:256
	global_load_dwordx4 v[184:187], v191, s[28:29] offset:2304
	s_waitcnt vmcnt(12)
	v_lshlrev_b32_e32 v220, 16, v192
	v_and_b32_e32 v221, 0xffff0000, v192
	v_lshlrev_b32_e32 v222, 16, v193
	v_and_b32_e32 v223, 0xffff0000, v193
	v_lshlrev_b32_e32 v224, 16, v194
	v_and_b32_e32 v225, 0xffff0000, v194
	v_lshlrev_b32_e32 v226, 16, v195
	v_and_b32_e32 v227, 0xffff0000, v195
	v_max_f32_e32 v220, 0x1e3ce508, v220
	v_max_f32_e32 v221, 0x1e3ce508, v221
	v_max_f32_e32 v222, 0x1e3ce508, v222
	v_max_f32_e32 v223, 0x1e3ce508, v223
	v_max_f32_e32 v224, 0x1e3ce508, v224
	v_max_f32_e32 v225, 0x1e3ce508, v225
	v_max_f32_e32 v226, 0x1e3ce508, v226
	v_max_f32_e32 v227, 0x1e3ce508, v227
	v_mov_b32_e32 v248, v196
	v_mov_b32_e32 v249, v197
	v_mov_b32_e32 v250, v198
	v_mov_b32_e32 v251, v199
	v_lshlrev_b32_e32 v192, 16, v196
	v_and_b32_e32 v193, 0xffff0000, v196
	v_lshlrev_b32_e32 v194, 16, v197
	v_and_b32_e32 v195, 0xffff0000, v197
	v_lshlrev_b32_e32 v196, 16, v198
	v_and_b32_e32 v197, 0xffff0000, v198
	v_lshlrev_b32_e32 v198, 16, v199
	v_and_b32_e32 v199, 0xffff0000, v199
	v_max_f32_e32 v192, 0x1e3ce508, v192
	v_max_f32_e32 v193, 0x1e3ce508, v193
	v_max_f32_e32 v194, 0x1e3ce508, v194
	v_max_f32_e32 v195, 0x1e3ce508, v195
	v_max_f32_e32 v196, 0x1e3ce508, v196
	v_max_f32_e32 v197, 0x1e3ce508, v197
	v_max_f32_e32 v198, 0x1e3ce508, v198
	v_max_f32_e32 v199, 0x1e3ce508, v199
	v_rcp_f32_e32 v192, v192
	v_rcp_f32_e32 v193, v193
	v_rcp_f32_e32 v194, v194
	v_rcp_f32_e32 v195, v195
	v_rcp_f32_e32 v196, v196
	v_rcp_f32_e32 v197, v197
	v_rcp_f32_e32 v198, v198
	v_rcp_f32_e32 v199, v199
	v_pk_mul_f32 v[220:221], v[220:221], v[192:193]
	v_pk_mul_f32 v[222:223], v[222:223], v[194:195]
	v_pk_mul_f32 v[224:225], v[224:225], v[196:197]
	v_pk_mul_f32 v[226:227], v[226:227], v[198:199]
	v_pk_mul_f32 v[64:65], v[64:65], v[220:221]
	v_pk_mul_f32 v[66:67], v[66:67], v[222:223]
	v_pk_mul_f32 v[60:61], v[60:61], v[224:225]
	v_pk_mul_f32 v[62:63], v[62:63], v[226:227]
	s_add_u32 s28, s26, 0xf0000
	s_addc_u32 s29, s27, 0
	global_load_dwordx4 v[192:195], v191, s[28:29]
	global_load_dwordx4 v[196:199], v191, s[28:29] offset:2048
	s_waitcnt vmcnt(12)
	v_lshlrev_b32_e32 v220, 16, v212
	v_and_b32_e32 v221, 0xffff0000, v212
	v_lshlrev_b32_e32 v222, 16, v213
	v_and_b32_e32 v223, 0xffff0000, v213
	v_lshlrev_b32_e32 v224, 16, v214
	v_and_b32_e32 v225, 0xffff0000, v214
	v_lshlrev_b32_e32 v226, 16, v215
	v_and_b32_e32 v227, 0xffff0000, v215
	v_max_f32_e32 v220, 0x1e3ce508, v220
	v_max_f32_e32 v221, 0x1e3ce508, v221
	v_max_f32_e32 v222, 0x1e3ce508, v222
	v_max_f32_e32 v223, 0x1e3ce508, v223
	v_max_f32_e32 v224, 0x1e3ce508, v224
	v_max_f32_e32 v225, 0x1e3ce508, v225
	v_max_f32_e32 v226, 0x1e3ce508, v226
	v_max_f32_e32 v227, 0x1e3ce508, v227
	v_mov_b32_e32 v168, v216
	v_mov_b32_e32 v169, v217
	v_mov_b32_e32 v170, v218
	v_mov_b32_e32 v171, v219
	v_lshlrev_b32_e32 v212, 16, v216
	v_and_b32_e32 v213, 0xffff0000, v216
	v_lshlrev_b32_e32 v214, 16, v217
	v_and_b32_e32 v215, 0xffff0000, v217
	v_lshlrev_b32_e32 v216, 16, v218
	v_and_b32_e32 v217, 0xffff0000, v218
	v_lshlrev_b32_e32 v218, 16, v219
	v_and_b32_e32 v219, 0xffff0000, v219
	v_max_f32_e32 v212, 0x1e3ce508, v212
	v_max_f32_e32 v213, 0x1e3ce508, v213
	v_max_f32_e32 v214, 0x1e3ce508, v214
	v_max_f32_e32 v215, 0x1e3ce508, v215
	v_max_f32_e32 v216, 0x1e3ce508, v216
	v_max_f32_e32 v217, 0x1e3ce508, v217
	v_max_f32_e32 v218, 0x1e3ce508, v218
	v_max_f32_e32 v219, 0x1e3ce508, v219
	v_rcp_f32_e32 v212, v212
	v_rcp_f32_e32 v213, v213
	v_rcp_f32_e32 v214, v214
	v_rcp_f32_e32 v215, v215
	v_rcp_f32_e32 v216, v216
	v_rcp_f32_e32 v217, v217
	v_rcp_f32_e32 v218, v218
	v_rcp_f32_e32 v219, v219
	v_pk_mul_f32 v[220:221], v[220:221], v[212:213]
	v_pk_mul_f32 v[222:223], v[222:223], v[214:215]
	v_pk_mul_f32 v[224:225], v[224:225], v[216:217]
	v_pk_mul_f32 v[226:227], v[226:227], v[218:219]
	v_pk_mul_f32 v[88:89], v[88:89], v[220:221]
	v_pk_mul_f32 v[90:91], v[90:91], v[222:223]
	v_pk_mul_f32 v[84:85], v[84:85], v[224:225]
	v_pk_mul_f32 v[86:87], v[86:87], v[226:227]
	s_add_u32 s28, s26, 0xf0000
	s_addc_u32 s29, s27, 0
	global_load_dwordx4 v[212:215], v191, s[28:29] offset:256
	global_load_dwordx4 v[216:219], v191, s[28:29] offset:2304
	s_waitcnt vmcnt(12)
	v_lshlrev_b32_e32 v220, 16, v132
	v_and_b32_e32 v221, 0xffff0000, v132
	v_lshlrev_b32_e32 v222, 16, v133
	v_and_b32_e32 v223, 0xffff0000, v133
	v_lshlrev_b32_e32 v224, 16, v134
	v_and_b32_e32 v225, 0xffff0000, v134
	v_lshlrev_b32_e32 v226, 16, v135
	v_and_b32_e32 v227, 0xffff0000, v135
	v_max_f32_e32 v220, 0x1e3ce508, v220
	v_max_f32_e32 v221, 0x1e3ce508, v221
	v_max_f32_e32 v222, 0x1e3ce508, v222
	v_max_f32_e32 v223, 0x1e3ce508, v223
	v_max_f32_e32 v224, 0x1e3ce508, v224
	v_max_f32_e32 v225, 0x1e3ce508, v225
	v_max_f32_e32 v226, 0x1e3ce508, v226
	v_max_f32_e32 v227, 0x1e3ce508, v227
	v_lshlrev_b32_e32 v132, 16, v136
	v_and_b32_e32 v133, 0xffff0000, v136
	v_lshlrev_b32_e32 v134, 16, v137
	v_and_b32_e32 v135, 0xffff0000, v137
	v_lshlrev_b32_e32 v136, 16, v138
	v_and_b32_e32 v137, 0xffff0000, v138
	v_lshlrev_b32_e32 v138, 16, v139
	v_and_b32_e32 v139, 0xffff0000, v139
	v_max_f32_e32 v132, 0x1e3ce508, v132
	v_max_f32_e32 v133, 0x1e3ce508, v133
	v_max_f32_e32 v134, 0x1e3ce508, v134
	v_max_f32_e32 v135, 0x1e3ce508, v135
	v_max_f32_e32 v136, 0x1e3ce508, v136
	v_max_f32_e32 v137, 0x1e3ce508, v137
	v_max_f32_e32 v138, 0x1e3ce508, v138
	v_max_f32_e32 v139, 0x1e3ce508, v139
	v_rcp_f32_e32 v132, v132
	v_rcp_f32_e32 v133, v133
	v_rcp_f32_e32 v134, v134
	v_rcp_f32_e32 v135, v135
	v_rcp_f32_e32 v136, v136
	v_rcp_f32_e32 v137, v137
	v_rcp_f32_e32 v138, v138
	v_rcp_f32_e32 v139, v139
	v_pk_mul_f32 v[220:221], v[220:221], v[132:133]
	v_pk_mul_f32 v[222:223], v[222:223], v[134:135]
	v_pk_mul_f32 v[224:225], v[224:225], v[136:137]
	v_pk_mul_f32 v[226:227], v[226:227], v[138:139]
	v_pk_mul_f32 v[56:57], v[56:57], v[220:221]
	v_pk_mul_f32 v[58:59], v[58:59], v[222:223]
	v_pk_mul_f32 v[48:49], v[48:49], v[224:225]
	v_pk_mul_f32 v[50:51], v[50:51], v[226:227]
	s_add_u32 s28, s26, 0x108000
	s_addc_u32 s29, s27, 0
	global_load_dwordx4 v[132:135], v191, s[28:29]
	global_load_dwordx4 v[136:139], v191, s[28:29] offset:2048
	s_waitcnt vmcnt(12)
	v_lshlrev_b32_e32 v220, 16, v140
	v_and_b32_e32 v221, 0xffff0000, v140
	v_lshlrev_b32_e32 v222, 16, v141
	v_and_b32_e32 v223, 0xffff0000, v141
	v_lshlrev_b32_e32 v224, 16, v142
	v_and_b32_e32 v225, 0xffff0000, v142
	v_lshlrev_b32_e32 v226, 16, v143
	v_and_b32_e32 v227, 0xffff0000, v143
	v_max_f32_e32 v220, 0x1e3ce508, v220
	v_max_f32_e32 v221, 0x1e3ce508, v221
	v_max_f32_e32 v222, 0x1e3ce508, v222
	v_max_f32_e32 v223, 0x1e3ce508, v223
	v_max_f32_e32 v224, 0x1e3ce508, v224
	v_max_f32_e32 v225, 0x1e3ce508, v225
	v_max_f32_e32 v226, 0x1e3ce508, v226
	v_max_f32_e32 v227, 0x1e3ce508, v227
	v_lshlrev_b32_e32 v140, 16, v144
	v_and_b32_e32 v141, 0xffff0000, v144
	v_lshlrev_b32_e32 v142, 16, v145
	v_and_b32_e32 v143, 0xffff0000, v145
	v_lshlrev_b32_e32 v144, 16, v146
	v_and_b32_e32 v145, 0xffff0000, v146
	v_lshlrev_b32_e32 v146, 16, v147
	v_and_b32_e32 v147, 0xffff0000, v147
	v_max_f32_e32 v140, 0x1e3ce508, v140
	v_max_f32_e32 v141, 0x1e3ce508, v141
	v_max_f32_e32 v142, 0x1e3ce508, v142
	v_max_f32_e32 v143, 0x1e3ce508, v143
	v_max_f32_e32 v144, 0x1e3ce508, v144
	v_max_f32_e32 v145, 0x1e3ce508, v145
	v_max_f32_e32 v146, 0x1e3ce508, v146
	v_max_f32_e32 v147, 0x1e3ce508, v147
	v_rcp_f32_e32 v140, v140
	v_rcp_f32_e32 v141, v141
	v_rcp_f32_e32 v142, v142
	v_rcp_f32_e32 v143, v143
	v_rcp_f32_e32 v144, v144
	v_rcp_f32_e32 v145, v145
	v_rcp_f32_e32 v146, v146
	v_rcp_f32_e32 v147, v147
	v_pk_mul_f32 v[220:221], v[220:221], v[140:141]
	v_pk_mul_f32 v[222:223], v[222:223], v[142:143]
	v_pk_mul_f32 v[224:225], v[224:225], v[144:145]
	v_pk_mul_f32 v[226:227], v[226:227], v[146:147]
	v_pk_mul_f32 v[52:53], v[52:53], v[220:221]
	v_pk_mul_f32 v[54:55], v[54:55], v[222:223]
	v_pk_mul_f32 v[44:45], v[44:45], v[224:225]
	v_pk_mul_f32 v[46:47], v[46:47], v[226:227]
	s_add_u32 s28, s26, 0x108000
	s_addc_u32 s29, s27, 0
	global_load_dwordx4 v[140:143], v191, s[28:29] offset:256
	global_load_dwordx4 v[144:147], v191, s[28:29] offset:2304
	s_waitcnt vmcnt(12)
	v_lshlrev_b32_e32 v220, 16, v148
	v_and_b32_e32 v221, 0xffff0000, v148
	v_lshlrev_b32_e32 v222, 16, v149
	v_and_b32_e32 v223, 0xffff0000, v149
	v_lshlrev_b32_e32 v224, 16, v150
	v_and_b32_e32 v225, 0xffff0000, v150
	v_lshlrev_b32_e32 v226, 16, v151
	v_and_b32_e32 v227, 0xffff0000, v151
	v_max_f32_e32 v220, 0x1e3ce508, v220
	v_max_f32_e32 v221, 0x1e3ce508, v221
	v_max_f32_e32 v222, 0x1e3ce508, v222
	v_max_f32_e32 v223, 0x1e3ce508, v223
	v_max_f32_e32 v224, 0x1e3ce508, v224
	v_max_f32_e32 v225, 0x1e3ce508, v225
	v_max_f32_e32 v226, 0x1e3ce508, v226
	v_max_f32_e32 v227, 0x1e3ce508, v227
	v_lshlrev_b32_e32 v148, 16, v152
	v_and_b32_e32 v149, 0xffff0000, v152
	v_lshlrev_b32_e32 v150, 16, v153
	v_and_b32_e32 v151, 0xffff0000, v153
	v_lshlrev_b32_e32 v152, 16, v154
	v_and_b32_e32 v153, 0xffff0000, v154
	v_lshlrev_b32_e32 v154, 16, v155
	v_and_b32_e32 v155, 0xffff0000, v155
	v_max_f32_e32 v148, 0x1e3ce508, v148
	v_max_f32_e32 v149, 0x1e3ce508, v149
	v_max_f32_e32 v150, 0x1e3ce508, v150
	v_max_f32_e32 v151, 0x1e3ce508, v151
	v_max_f32_e32 v152, 0x1e3ce508, v152
	v_max_f32_e32 v153, 0x1e3ce508, v153
	v_max_f32_e32 v154, 0x1e3ce508, v154
	v_max_f32_e32 v155, 0x1e3ce508, v155
	v_rcp_f32_e32 v148, v148
	v_rcp_f32_e32 v149, v149
	v_rcp_f32_e32 v150, v150
	v_rcp_f32_e32 v151, v151
	v_rcp_f32_e32 v152, v152
	v_rcp_f32_e32 v153, v153
	v_rcp_f32_e32 v154, v154
	v_rcp_f32_e32 v155, v155
	v_pk_mul_f32 v[220:221], v[220:221], v[148:149]
	v_pk_mul_f32 v[222:223], v[222:223], v[150:151]
	v_pk_mul_f32 v[224:225], v[224:225], v[152:153]
	v_pk_mul_f32 v[226:227], v[226:227], v[154:155]
	v_pk_mul_f32 v[16:17], v[16:17], v[220:221]
	v_pk_mul_f32 v[18:19], v[18:19], v[222:223]
	v_pk_mul_f32 v[12:13], v[12:13], v[224:225]
	v_pk_mul_f32 v[14:15], v[14:15], v[226:227]
	s_waitcnt vmcnt(10)
	v_lshlrev_b32_e32 v220, 16, v156
	v_and_b32_e32 v221, 0xffff0000, v156
	v_lshlrev_b32_e32 v222, 16, v157
	v_and_b32_e32 v223, 0xffff0000, v157
	v_lshlrev_b32_e32 v224, 16, v158
	v_and_b32_e32 v225, 0xffff0000, v158
	v_lshlrev_b32_e32 v226, 16, v159
	v_and_b32_e32 v227, 0xffff0000, v159
	v_max_f32_e32 v220, 0x1e3ce508, v220
	v_max_f32_e32 v221, 0x1e3ce508, v221
	v_max_f32_e32 v222, 0x1e3ce508, v222
	v_max_f32_e32 v223, 0x1e3ce508, v223
	v_max_f32_e32 v224, 0x1e3ce508, v224
	v_max_f32_e32 v225, 0x1e3ce508, v225
	v_max_f32_e32 v226, 0x1e3ce508, v226
	v_max_f32_e32 v227, 0x1e3ce508, v227
	v_lshlrev_b32_e32 v156, 16, v160
	v_and_b32_e32 v157, 0xffff0000, v160
	v_lshlrev_b32_e32 v158, 16, v161
	v_and_b32_e32 v159, 0xffff0000, v161
	v_lshlrev_b32_e32 v160, 16, v162
	v_and_b32_e32 v161, 0xffff0000, v162
	v_lshlrev_b32_e32 v162, 16, v163
	v_and_b32_e32 v163, 0xffff0000, v163
	v_max_f32_e32 v156, 0x1e3ce508, v156
	v_max_f32_e32 v157, 0x1e3ce508, v157
	v_max_f32_e32 v158, 0x1e3ce508, v158
	v_max_f32_e32 v159, 0x1e3ce508, v159
	v_max_f32_e32 v160, 0x1e3ce508, v160
	v_max_f32_e32 v161, 0x1e3ce508, v161
	v_max_f32_e32 v162, 0x1e3ce508, v162
	v_max_f32_e32 v163, 0x1e3ce508, v163
	v_rcp_f32_e32 v156, v156
	v_rcp_f32_e32 v157, v157
	v_rcp_f32_e32 v158, v158
	v_rcp_f32_e32 v159, v159
	v_rcp_f32_e32 v160, v160
	v_rcp_f32_e32 v161, v161
	v_rcp_f32_e32 v162, v162
	v_rcp_f32_e32 v163, v163
	v_pk_mul_f32 v[220:221], v[220:221], v[156:157]
	v_pk_mul_f32 v[222:223], v[222:223], v[158:159]
	v_pk_mul_f32 v[224:225], v[224:225], v[160:161]
	v_pk_mul_f32 v[226:227], v[226:227], v[162:163]
	v_pk_mul_f32 v[40:41], v[40:41], v[220:221]
	v_pk_mul_f32 v[42:43], v[42:43], v[222:223]
	v_pk_mul_f32 v[36:37], v[36:37], v[224:225]
	v_pk_mul_f32 v[38:39], v[38:39], v[226:227]
	s_waitcnt vmcnt(8)
	v_lshlrev_b32_e32 v220, 16, v180
	v_and_b32_e32 v221, 0xffff0000, v180
	v_lshlrev_b32_e32 v222, 16, v181
	v_and_b32_e32 v223, 0xffff0000, v181
	v_lshlrev_b32_e32 v224, 16, v182
	v_and_b32_e32 v225, 0xffff0000, v182
	v_lshlrev_b32_e32 v226, 16, v183
	v_and_b32_e32 v227, 0xffff0000, v183
	v_max_f32_e32 v220, 0x1e3ce508, v220
	v_max_f32_e32 v221, 0x1e3ce508, v221
	v_max_f32_e32 v222, 0x1e3ce508, v222
	v_max_f32_e32 v223, 0x1e3ce508, v223
	v_max_f32_e32 v224, 0x1e3ce508, v224
	v_max_f32_e32 v225, 0x1e3ce508, v225
	v_max_f32_e32 v226, 0x1e3ce508, v226
	v_max_f32_e32 v227, 0x1e3ce508, v227
	v_lshlrev_b32_e32 v180, 16, v184
	v_and_b32_e32 v181, 0xffff0000, v184
	v_lshlrev_b32_e32 v182, 16, v185
	v_and_b32_e32 v183, 0xffff0000, v185
	v_lshlrev_b32_e32 v184, 16, v186
	v_and_b32_e32 v185, 0xffff0000, v186
	v_lshlrev_b32_e32 v186, 16, v187
	v_and_b32_e32 v187, 0xffff0000, v187
	v_max_f32_e32 v180, 0x1e3ce508, v180
	v_max_f32_e32 v181, 0x1e3ce508, v181
	v_max_f32_e32 v182, 0x1e3ce508, v182
	v_max_f32_e32 v183, 0x1e3ce508, v183
	v_max_f32_e32 v184, 0x1e3ce508, v184
	v_max_f32_e32 v185, 0x1e3ce508, v185
	v_max_f32_e32 v186, 0x1e3ce508, v186
	v_max_f32_e32 v187, 0x1e3ce508, v187
	v_rcp_f32_e32 v180, v180
	v_rcp_f32_e32 v181, v181
	v_rcp_f32_e32 v182, v182
	v_rcp_f32_e32 v183, v183
	v_rcp_f32_e32 v184, v184
	v_rcp_f32_e32 v185, v185
	v_rcp_f32_e32 v186, v186
	v_rcp_f32_e32 v187, v187
	v_pk_mul_f32 v[220:221], v[220:221], v[180:181]
	v_pk_mul_f32 v[222:223], v[222:223], v[182:183]
	v_pk_mul_f32 v[224:225], v[224:225], v[184:185]
	v_pk_mul_f32 v[226:227], v[226:227], v[186:187]
	v_pk_mul_f32 v[8:9], v[8:9], v[220:221]
	v_pk_mul_f32 v[10:11], v[10:11], v[222:223]
	v_pk_mul_f32 v[4:5], v[4:5], v[224:225]
	v_pk_mul_f32 v[6:7], v[6:7], v[226:227]
	s_waitcnt vmcnt(6)
	v_lshlrev_b32_e32 v220, 16, v192
	v_and_b32_e32 v221, 0xffff0000, v192
	v_lshlrev_b32_e32 v222, 16, v193
	v_and_b32_e32 v223, 0xffff0000, v193
	v_lshlrev_b32_e32 v224, 16, v194
	v_and_b32_e32 v225, 0xffff0000, v194
	v_lshlrev_b32_e32 v226, 16, v195
	v_and_b32_e32 v227, 0xffff0000, v195
	v_max_f32_e32 v220, 0x1e3ce508, v220
	v_max_f32_e32 v221, 0x1e3ce508, v221
	v_max_f32_e32 v222, 0x1e3ce508, v222
	v_max_f32_e32 v223, 0x1e3ce508, v223
	v_max_f32_e32 v224, 0x1e3ce508, v224
	v_max_f32_e32 v225, 0x1e3ce508, v225
	v_max_f32_e32 v226, 0x1e3ce508, v226
	v_max_f32_e32 v227, 0x1e3ce508, v227
	v_lshlrev_b32_e32 v192, 16, v196
	v_and_b32_e32 v193, 0xffff0000, v196
	v_lshlrev_b32_e32 v194, 16, v197
	v_and_b32_e32 v195, 0xffff0000, v197
	v_lshlrev_b32_e32 v196, 16, v198
	v_and_b32_e32 v197, 0xffff0000, v198
	v_lshlrev_b32_e32 v198, 16, v199
	v_and_b32_e32 v199, 0xffff0000, v199
	v_max_f32_e32 v192, 0x1e3ce508, v192
	v_max_f32_e32 v193, 0x1e3ce508, v193
	v_max_f32_e32 v194, 0x1e3ce508, v194
	v_max_f32_e32 v195, 0x1e3ce508, v195
	v_max_f32_e32 v196, 0x1e3ce508, v196
	v_max_f32_e32 v197, 0x1e3ce508, v197
	v_max_f32_e32 v198, 0x1e3ce508, v198
	v_max_f32_e32 v199, 0x1e3ce508, v199
	v_rcp_f32_e32 v192, v192
	v_rcp_f32_e32 v193, v193
	v_rcp_f32_e32 v194, v194
	v_rcp_f32_e32 v195, v195
	v_rcp_f32_e32 v196, v196
	v_rcp_f32_e32 v197, v197
	v_rcp_f32_e32 v198, v198
	v_rcp_f32_e32 v199, v199
	v_pk_mul_f32 v[220:221], v[220:221], v[192:193]
	v_pk_mul_f32 v[222:223], v[222:223], v[194:195]
	v_pk_mul_f32 v[224:225], v[224:225], v[196:197]
	v_pk_mul_f32 v[226:227], v[226:227], v[198:199]
	v_pk_mul_f32 v[32:33], v[32:33], v[220:221]
	v_pk_mul_f32 v[34:35], v[34:35], v[222:223]
	v_pk_mul_f32 v[28:29], v[28:29], v[224:225]
	v_pk_mul_f32 v[30:31], v[30:31], v[226:227]
	s_waitcnt vmcnt(4)
	v_lshlrev_b32_e32 v220, 16, v212
	v_and_b32_e32 v221, 0xffff0000, v212
	v_lshlrev_b32_e32 v222, 16, v213
	v_and_b32_e32 v223, 0xffff0000, v213
	v_lshlrev_b32_e32 v224, 16, v214
	v_and_b32_e32 v225, 0xffff0000, v214
	v_lshlrev_b32_e32 v226, 16, v215
	v_and_b32_e32 v227, 0xffff0000, v215
	v_max_f32_e32 v220, 0x1e3ce508, v220
	v_max_f32_e32 v221, 0x1e3ce508, v221
	v_max_f32_e32 v222, 0x1e3ce508, v222
	v_max_f32_e32 v223, 0x1e3ce508, v223
	v_max_f32_e32 v224, 0x1e3ce508, v224
	v_max_f32_e32 v225, 0x1e3ce508, v225
	v_max_f32_e32 v226, 0x1e3ce508, v226
	v_max_f32_e32 v227, 0x1e3ce508, v227
	v_lshlrev_b32_e32 v212, 16, v216
	v_and_b32_e32 v213, 0xffff0000, v216
	v_lshlrev_b32_e32 v214, 16, v217
	v_and_b32_e32 v215, 0xffff0000, v217
	v_lshlrev_b32_e32 v216, 16, v218
	v_and_b32_e32 v217, 0xffff0000, v218
	v_lshlrev_b32_e32 v218, 16, v219
	v_and_b32_e32 v219, 0xffff0000, v219
	v_max_f32_e32 v212, 0x1e3ce508, v212
	v_max_f32_e32 v213, 0x1e3ce508, v213
	v_max_f32_e32 v214, 0x1e3ce508, v214
	v_max_f32_e32 v215, 0x1e3ce508, v215
	v_max_f32_e32 v216, 0x1e3ce508, v216
	v_max_f32_e32 v217, 0x1e3ce508, v217
	v_max_f32_e32 v218, 0x1e3ce508, v218
	v_max_f32_e32 v219, 0x1e3ce508, v219
	v_rcp_f32_e32 v212, v212
	v_rcp_f32_e32 v213, v213
	v_rcp_f32_e32 v214, v214
	v_rcp_f32_e32 v215, v215
	v_rcp_f32_e32 v216, v216
	v_rcp_f32_e32 v217, v217
	v_rcp_f32_e32 v218, v218
	v_rcp_f32_e32 v219, v219
	v_pk_mul_f32 v[220:221], v[220:221], v[212:213]
	v_pk_mul_f32 v[222:223], v[222:223], v[214:215]
	v_pk_mul_f32 v[224:225], v[224:225], v[216:217]
	v_pk_mul_f32 v[226:227], v[226:227], v[218:219]
	v_pk_mul_f32 v[116:117], v[116:117], v[220:221]
	v_pk_mul_f32 v[118:119], v[118:119], v[222:223]
	v_pk_mul_f32 v[120:121], v[120:121], v[224:225]
	v_pk_mul_f32 v[122:123], v[122:123], v[226:227]
	s_waitcnt vmcnt(2)
	v_lshlrev_b32_e32 v220, 16, v132
	v_and_b32_e32 v221, 0xffff0000, v132
	v_lshlrev_b32_e32 v222, 16, v133
	v_and_b32_e32 v223, 0xffff0000, v133
	v_lshlrev_b32_e32 v224, 16, v134
	v_and_b32_e32 v225, 0xffff0000, v134
	v_lshlrev_b32_e32 v226, 16, v135
	v_and_b32_e32 v227, 0xffff0000, v135
	v_max_f32_e32 v220, 0x1e3ce508, v220
	v_max_f32_e32 v221, 0x1e3ce508, v221
	v_max_f32_e32 v222, 0x1e3ce508, v222
	v_max_f32_e32 v223, 0x1e3ce508, v223
	v_max_f32_e32 v224, 0x1e3ce508, v224
	v_max_f32_e32 v225, 0x1e3ce508, v225
	v_max_f32_e32 v226, 0x1e3ce508, v226
	v_max_f32_e32 v227, 0x1e3ce508, v227
	v_lshlrev_b32_e32 v132, 16, v136
	v_and_b32_e32 v133, 0xffff0000, v136
	v_lshlrev_b32_e32 v134, 16, v137
	v_and_b32_e32 v135, 0xffff0000, v137
	v_lshlrev_b32_e32 v136, 16, v138
	v_and_b32_e32 v137, 0xffff0000, v138
	v_lshlrev_b32_e32 v138, 16, v139
	v_and_b32_e32 v139, 0xffff0000, v139
	v_max_f32_e32 v132, 0x1e3ce508, v132
	v_max_f32_e32 v133, 0x1e3ce508, v133
	v_max_f32_e32 v134, 0x1e3ce508, v134
	v_max_f32_e32 v135, 0x1e3ce508, v135
	v_max_f32_e32 v136, 0x1e3ce508, v136
	v_max_f32_e32 v137, 0x1e3ce508, v137
	v_max_f32_e32 v138, 0x1e3ce508, v138
	v_max_f32_e32 v139, 0x1e3ce508, v139
	v_rcp_f32_e32 v132, v132
	v_rcp_f32_e32 v133, v133
	v_rcp_f32_e32 v134, v134
	v_rcp_f32_e32 v135, v135
	v_rcp_f32_e32 v136, v136
	v_rcp_f32_e32 v137, v137
	v_rcp_f32_e32 v138, v138
	v_rcp_f32_e32 v139, v139
	v_pk_mul_f32 v[220:221], v[220:221], v[132:133]
	v_pk_mul_f32 v[222:223], v[222:223], v[134:135]
	v_pk_mul_f32 v[224:225], v[224:225], v[136:137]
	v_pk_mul_f32 v[226:227], v[226:227], v[138:139]
	v_pk_mul_f32 v[24:25], v[24:25], v[220:221]
	v_pk_mul_f32 v[26:27], v[26:27], v[222:223]
	v_pk_mul_f32 v[20:21], v[20:21], v[224:225]
	v_pk_mul_f32 v[22:23], v[22:23], v[226:227]
	s_waitcnt vmcnt(0)
	v_lshlrev_b32_e32 v220, 16, v140
	v_and_b32_e32 v221, 0xffff0000, v140
	v_lshlrev_b32_e32 v222, 16, v141
	v_and_b32_e32 v223, 0xffff0000, v141
	v_lshlrev_b32_e32 v224, 16, v142
	v_and_b32_e32 v225, 0xffff0000, v142
	v_lshlrev_b32_e32 v226, 16, v143
	v_and_b32_e32 v227, 0xffff0000, v143
	v_max_f32_e32 v220, 0x1e3ce508, v220
	v_max_f32_e32 v221, 0x1e3ce508, v221
	v_max_f32_e32 v222, 0x1e3ce508, v222
	v_max_f32_e32 v223, 0x1e3ce508, v223
	v_max_f32_e32 v224, 0x1e3ce508, v224
	v_max_f32_e32 v225, 0x1e3ce508, v225
	v_max_f32_e32 v226, 0x1e3ce508, v226
	v_max_f32_e32 v227, 0x1e3ce508, v227
	v_lshlrev_b32_e32 v140, 16, v144
	v_and_b32_e32 v141, 0xffff0000, v144
	v_lshlrev_b32_e32 v142, 16, v145
	v_and_b32_e32 v143, 0xffff0000, v145
	v_lshlrev_b32_e32 v144, 16, v146
	v_and_b32_e32 v145, 0xffff0000, v146
	v_lshlrev_b32_e32 v146, 16, v147
	v_and_b32_e32 v147, 0xffff0000, v147
	v_max_f32_e32 v140, 0x1e3ce508, v140
	v_max_f32_e32 v141, 0x1e3ce508, v141
	v_max_f32_e32 v142, 0x1e3ce508, v142
	v_max_f32_e32 v143, 0x1e3ce508, v143
	v_max_f32_e32 v144, 0x1e3ce508, v144
	v_max_f32_e32 v145, 0x1e3ce508, v145
	v_max_f32_e32 v146, 0x1e3ce508, v146
	v_max_f32_e32 v147, 0x1e3ce508, v147
	v_rcp_f32_e32 v140, v140
	v_rcp_f32_e32 v141, v141
	v_rcp_f32_e32 v142, v142
	v_rcp_f32_e32 v143, v143
	v_rcp_f32_e32 v144, v144
	v_rcp_f32_e32 v145, v145
	v_rcp_f32_e32 v146, v146
	v_rcp_f32_e32 v147, v147
	v_pk_mul_f32 v[220:221], v[220:221], v[140:141]
	v_pk_mul_f32 v[222:223], v[222:223], v[142:143]
	v_pk_mul_f32 v[224:225], v[224:225], v[144:145]
	v_pk_mul_f32 v[226:227], v[226:227], v[146:147]
	v_pk_mul_f32 v[124:125], v[124:125], v[220:221]
	v_pk_mul_f32 v[126:127], v[126:127], v[222:223]
	v_pk_mul_f32 v[128:129], v[128:129], v[224:225]
	v_pk_mul_f32 v[130:131], v[130:131], v[226:227]
	s_branch .Lmg_done
.Lmg_mid:
	s_add_u32 s28, s26, 0x0
	s_addc_u32 s29, s27, 0
	global_load_dwordx4 v[136:139], v191, s[28:29] offset:2048
	s_add_u32 s28, s26, 0x0
	s_addc_u32 s29, s27, 0
	global_load_dwordx4 v[144:147], v191, s[28:29] offset:2304
	s_add_u32 s28, s26, 0x18000
	s_addc_u32 s29, s27, 0
	global_load_dwordx4 v[152:155], v191, s[28:29] offset:2048
	s_add_u32 s28, s26, 0x18000
	s_addc_u32 s29, s27, 0
	global_load_dwordx4 v[160:163], v191, s[28:29] offset:2304
	s_add_u32 s28, s26, 0x30000
	s_addc_u32 s29, s27, 0
	global_load_dwordx4 v[184:187], v191, s[28:29] offset:2048
	s_add_u32 s28, s26, 0x30000
	s_addc_u32 s29, s27, 0
	global_load_dwordx4 v[196:199], v191, s[28:29] offset:2304
	s_add_u32 s28, s26, 0x48000
	s_addc_u32 s29, s27, 0
	global_load_dwordx4 v[216:219], v191, s[28:29] offset:2048
	s_and_b64 vcc, exec, s[20:21]
	s_cbranch_vccz .Lmg_nbm
	s_barrier
.Lmg_nbm:
	s_waitcnt vmcnt(6)
	v_lshlrev_b32_e32 v220, 16, v228
	v_and_b32_e32 v221, 0xffff0000, v228
	v_lshlrev_b32_e32 v222, 16, v229
	v_and_b32_e32 v223, 0xffff0000, v229
	v_lshlrev_b32_e32 v224, 16, v230
	v_and_b32_e32 v225, 0xffff0000, v230
	v_lshlrev_b32_e32 v226, 16, v231
	v_and_b32_e32 v227, 0xffff0000, v231
	v_max_f32_e32 v220, 0x1e3ce508, v220
	v_max_f32_e32 v221, 0x1e3ce508, v221
	v_max_f32_e32 v222, 0x1e3ce508, v222
	v_max_f32_e32 v223, 0x1e3ce508, v223
	v_max_f32_e32 v224, 0x1e3ce508, v224
	v_max_f32_e32 v225, 0x1e3ce508, v225
	v_max_f32_e32 v226, 0x1e3ce508, v226
	v_max_f32_e32 v227, 0x1e3ce508, v227
	v_mov_b32_e32 v228, v136
	v_mov_b32_e32 v229, v137
	v_mov_b32_e32 v230, v138
	v_mov_b32_e32 v231, v139
	v_lshlrev_b32_e32 v132, 16, v136
	v_and_b32_e32 v133, 0xffff0000, v136
	v_lshlrev_b32_e32 v134, 16, v137
	v_and_b32_e32 v135, 0xffff0000, v137
	v_lshlrev_b32_e32 v136, 16, v138
	v_and_b32_e32 v137, 0xffff0000, v138
	v_lshlrev_b32_e32 v138, 16, v139
	v_and_b32_e32 v139, 0xffff0000, v139
	v_max_f32_e32 v132, 0x1e3ce508, v132
	v_max_f32_e32 v133, 0x1e3ce508, v133
	v_max_f32_e32 v134, 0x1e3ce508, v134
	v_max_f32_e32 v135, 0x1e3ce508, v135
	v_max_f32_e32 v136, 0x1e3ce508, v136
	v_max_f32_e32 v137, 0x1e3ce508, v137
	v_max_f32_e32 v138, 0x1e3ce508, v138
	v_max_f32_e32 v139, 0x1e3ce508, v139
	v_rcp_f32_e32 v132, v132
	v_rcp_f32_e32 v133, v133
	v_rcp_f32_e32 v134, v134
	v_rcp_f32_e32 v135, v135
	v_rcp_f32_e32 v136, v136
	v_rcp_f32_e32 v137, v137
	v_rcp_f32_e32 v138, v138
	v_rcp_f32_e32 v139, v139
	v_pk_mul_f32 v[220:221], v[220:221], v[132:133]
	v_pk_mul_f32 v[222:223], v[222:223], v[134:135]
	v_pk_mul_f32 v[224:225], v[224:225], v[136:137]
	v_pk_mul_f32 v[226:227], v[226:227], v[138:139]
	v_pk_mul_f32 v[112:113], v[112:113], v[220:221]
	v_pk_mul_f32 v[114:115], v[114:115], v[222:223]
	v_pk_mul_f32 v[108:109], v[108:109], v[224:225]
	v_pk_mul_f32 v[110:111], v[110:111], v[226:227]
	s_add_u32 s28, s26, 0x48000
	s_addc_u32 s29, s27, 0
	global_load_dwordx4 v[132:135], v191, s[28:29] offset:256
	global_load_dwordx4 v[136:139], v191, s[28:29] offset:2304
	s_waitcnt vmcnt(7)
	v_lshlrev_b32_e32 v220, 16, v232
	v_and_b32_e32 v221, 0xffff0000, v232
	v_lshlrev_b32_e32 v222, 16, v233
	v_and_b32_e32 v223, 0xffff0000, v233
	v_lshlrev_b32_e32 v224, 16, v234
	v_and_b32_e32 v225, 0xffff0000, v234
	v_lshlrev_b32_e32 v226, 16, v235
	v_and_b32_e32 v227, 0xffff0000, v235
	v_max_f32_e32 v220, 0x1e3ce508, v220
	v_max_f32_e32 v221, 0x1e3ce508, v221
	v_max_f32_e32 v222, 0x1e3ce508, v222
	v_max_f32_e32 v223, 0x1e3ce508, v223
	v_max_f32_e32 v224, 0x1e3ce508, v224
	v_max_f32_e32 v225, 0x1e3ce508, v225
	v_max_f32_e32 v226, 0x1e3ce508, v226
	v_max_f32_e32 v227, 0x1e3ce508, v227
	v_mov_b32_e32 v232, v144
	v_mov_b32_e32 v233, v145
	v_mov_b32_e32 v234, v146
	v_mov_b32_e32 v235, v147
	v_lshlrev_b32_e32 v140, 16, v144
	v_and_b32_e32 v141, 0xffff0000, v144
	v_lshlrev_b32_e32 v142, 16, v145
	v_and_b32_e32 v143, 0xffff0000, v145
	v_lshlrev_b32_e32 v144, 16, v146
	v_and_b32_e32 v145, 0xffff0000, v146
	v_lshlrev_b32_e32 v146, 16, v147
	v_and_b32_e32 v147, 0xffff0000, v147
	v_max_f32_e32 v140, 0x1e3ce508, v140
	v_max_f32_e32 v141, 0x1e3ce508, v141
	v_max_f32_e32 v142, 0x1e3ce508, v142
	v_max_f32_e32 v143, 0x1e3ce508, v143
	v_max_f32_e32 v144, 0x1e3ce508, v144
	v_max_f32_e32 v145, 0x1e3ce508, v145
	v_max_f32_e32 v146, 0x1e3ce508, v146
	v_max_f32_e32 v147, 0x1e3ce508, v147
	v_rcp_f32_e32 v140, v140
	v_rcp_f32_e32 v141, v141
	v_rcp_f32_e32 v142, v142
	v_rcp_f32_e32 v143, v143
	v_rcp_f32_e32 v144, v144
	v_rcp_f32_e32 v145, v145
	v_rcp_f32_e32 v146, v146
	v_rcp_f32_e32 v147, v147
	v_pk_mul_f32 v[220:221], v[220:221], v[140:141]
	v_pk_mul_f32 v[222:223], v[222:223], v[142:143]
	v_pk_mul_f32 v[224:225], v[224:225], v[144:145]
	v_pk_mul_f32 v[226:227], v[226:227], v[146:147]
	v_pk_mul_f32 v[80:81], v[80:81], v[220:221]
	v_pk_mul_f32 v[82:83], v[82:83], v[222:223]
	v_pk_mul_f32 v[76:77], v[76:77], v[224:225]
	v_pk_mul_f32 v[78:79], v[78:79], v[226:227]
	s_add_u32 s28, s26, 0xc0000
	s_addc_u32 s29, s27, 0
	global_load_dwordx4 v[140:143], v191, s[28:29]
	global_load_dwordx4 v[144:147], v191, s[28:29] offset:2048
	s_waitcnt vmcnt(8)
	v_lshlrev_b32_e32 v220, 16, v236
	v_and_b32_e32 v221, 0xffff0000, v236
	v_lshlrev_b32_e32 v222, 16, v237
	v_and_b32_e32 v223, 0xffff0000, v237
	v_lshlrev_b32_e32 v224, 16, v238
	v_and_b32_e32 v225, 0xffff0000, v238
	v_lshlrev_b32_e32 v226, 16, v239
	v_and_b32_e32 v227, 0xffff0000, v239
	v_max_f32_e32 v220, 0x1e3ce508, v220
	v_max_f32_e32 v221, 0x1e3ce508, v221
	v_max_f32_e32 v222, 0x1e3ce508, v222
	v_max_f32_e32 v223, 0x1e3ce508, v223
	v_max_f32_e32 v224, 0x1e3ce508, v224
	v_max_f32_e32 v225, 0x1e3ce508, v225
	v_max_f32_e32 v226, 0x1e3ce508, v226
	v_max_f32_e32 v227, 0x1e3ce508, v227
	v_mov_b32_e32 v236, v152
	v_mov_b32_e32 v237, v153
	v_mov_b32_e32 v238, v154
	v_mov_b32_e32 v239, v155
	v_lshlrev_b32_e32 v148, 16, v152
	v_and_b32_e32 v149, 0xffff0000, v152
	v_lshlrev_b32_e32 v150, 16, v153
	v_and_b32_e32 v151, 0xffff0000, v153
	v_lshlrev_b32_e32 v152, 16, v154
	v_and_b32_e32 v153, 0xffff0000, v154
	v_lshlrev_b32_e32 v154, 16, v155
	v_and_b32_e32 v155, 0xffff0000, v155
	v_max_f32_e32 v148, 0x1e3ce508, v148
	v_max_f32_e32 v149, 0x1e3ce508, v149
	v_max_f32_e32 v150, 0x1e3ce508, v150
	v_max_f32_e32 v151, 0x1e3ce508, v151
	v_max_f32_e32 v152, 0x1e3ce508, v152
	v_max_f32_e32 v153, 0x1e3ce508, v153
	v_max_f32_e32 v154, 0x1e3ce508, v154
	v_max_f32_e32 v155, 0x1e3ce508, v155
	v_rcp_f32_e32 v148, v148
	v_rcp_f32_e32 v149, v149
	v_rcp_f32_e32 v150, v150
	v_rcp_f32_e32 v151, v151
	v_rcp_f32_e32 v152, v152
	v_rcp_f32_e32 v153, v153
	v_rcp_f32_e32 v154, v154
	v_rcp_f32_e32 v155, v155
	v_pk_mul_f32 v[220:221], v[220:221], v[148:149]
	v_pk_mul_f32 v[222:223], v[222:223], v[150:151]
	v_pk_mul_f32 v[224:225], v[224:225], v[152:153]
	v_pk_mul_f32 v[226:227], v[226:227], v[154:155]
	v_pk_mul_f32 v[104:105], v[104:105], v[220:221]
	v_pk_mul_f32 v[106:107], v[106:107], v[222:223]
	v_pk_mul_f32 v[100:101], v[100:101], v[224:225]
	v_pk_mul_f32 v[102:103], v[102:103], v[226:227]
	s_add_u32 s28, s26, 0xc0000
	s_addc_u32 s29, s27, 0
	global_load_dwordx4 v[148:151], v191, s[28:29] offset:256
	global_load_dwordx4 v[152:155], v191, s[28:29] offset:2304
	s_waitcnt vmcnt(9)
	v_lshlrev_b32_e32 v220, 16, v240
	v_and_b32_e32 v221, 0xffff0000, v240
	v_lshlrev_b32_e32 v222, 16, v241
	v_and_b32_e32 v223, 0xffff0000, v241
	v_lshlrev_b32_e32 v224, 16, v242
	v_and_b32_e32 v225, 0xffff0000, v242
	v_lshlrev_b32_e32 v226, 16, v243
	v_and_b32_e32 v227, 0xffff0000, v243
	v_max_f32_e32 v220, 0x1e3ce508, v220
	v_max_f32_e32 v221, 0x1e3ce508, v221
	v_max_f32_e32 v222, 0x1e3ce508, v222
	v_max_f32_e32 v223, 0x1e3ce508, v223
	v_max_f32_e32 v224, 0x1e3ce508, v224
	v_max_f32_e32 v225, 0x1e3ce508, v225
	v_max_f32_e32 v226, 0x1e3ce508, v226
	v_max_f32_e32 v227, 0x1e3ce508, v227
	v_mov_b32_e32 v240, v160
	v_mov_b32_e32 v241, v161
	v_mov_b32_e32 v242, v162
	v_mov_b32_e32 v243, v163
	v_lshlrev_b32_e32 v156, 16, v160
	v_and_b32_e32 v157, 0xffff0000, v160
	v_lshlrev_b32_e32 v158, 16, v161
	v_and_b32_e32 v159, 0xffff0000, v161
	v_lshlrev_b32_e32 v160, 16, v162
	v_and_b32_e32 v161, 0xffff0000, v162
	v_lshlrev_b32_e32 v162, 16, v163
	v_and_b32_e32 v163, 0xffff0000, v163
	v_max_f32_e32 v156, 0x1e3ce508, v156
	v_max_f32_e32 v157, 0x1e3ce508, v157
	v_max_f32_e32 v158, 0x1e3ce508, v158
	v_max_f32_e32 v159, 0x1e3ce508, v159
	v_max_f32_e32 v160, 0x1e3ce508, v160
	v_max_f32_e32 v161, 0x1e3ce508, v161
	v_max_f32_e32 v162, 0x1e3ce508, v162
	v_max_f32_e32 v163, 0x1e3ce508, v163
	v_rcp_f32_e32 v156, v156
	v_rcp_f32_e32 v157, v157
	v_rcp_f32_e32 v158, v158
	v_rcp_f32_e32 v159, v159
	v_rcp_f32_e32 v160, v160
	v_rcp_f32_e32 v161, v161
	v_rcp_f32_e32 v162, v162
	v_rcp_f32_e32 v163, v163
	v_pk_mul_f32 v[220:221], v[220:221], v[156:157]
	v_pk_mul_f32 v[222:223], v[222:223], v[158:159]
	v_pk_mul_f32 v[224:225], v[224:225], v[160:161]
	v_pk_mul_f32 v[226:227], v[226:227], v[162:163]
	v_pk_mul_f32 v[72:73], v[72:73], v[220:221]
	v_pk_mul_f32 v[74:75], v[74:75], v[222:223]
	v_pk_mul_f32 v[68:69], v[68:69], v[224:225]
	v_pk_mul_f32 v[70:71], v[70:71], v[226:227]
	s_add_u32 s28, s26, 0xd8000
	s_addc_u32 s29, s27, 0
	global_load_dwordx4 v[156:159], v191, s[28:29]
	global_load_dwordx4 v[160:163], v191, s[28:29] offset:2048
	s_waitcnt vmcnt(10)
	v_lshlrev_b32_e32 v220, 16, v244
	v_and_b32_e32 v221, 0xffff0000, v244
	v_lshlrev_b32_e32 v222, 16, v245
	v_and_b32_e32 v223, 0xffff0000, v245
	v_lshlrev_b32_e32 v224, 16, v246
	v_and_b32_e32 v225, 0xffff0000, v246
	v_lshlrev_b32_e32 v226, 16, v247
	v_and_b32_e32 v227, 0xffff0000, v247
	v_max_f32_e32 v220, 0x1e3ce508, v220
	v_max_f32_e32 v221, 0x1e3ce508, v221
	v_max_f32_e32 v222, 0x1e3ce508, v222
	v_max_f32_e32 v223, 0x1e3ce508, v223
	v_max_f32_e32 v224, 0x1e3ce508, v224
	v_max_f32_e32 v225, 0x1e3ce508, v225
	v_max_f32_e32 v226, 0x1e3ce508, v226
	v_max_f32_e32 v227, 0x1e3ce508, v227
	v_mov_b32_e32 v244, v184
	v_mov_b32_e32 v245, v185
	v_mov_b32_e32 v246, v186
	v_mov_b32_e32 v247, v187
	v_lshlrev_b32_e32 v180, 16, v184
	v_and_b32_e32 v181, 0xffff0000, v184
	v_lshlrev_b32_e32 v182, 16, v185
	v_and_b32_e32 v183, 0xffff0000, v185
	v_lshlrev_b32_e32 v184, 16, v186
	v_and_b32_e32 v185, 0xffff0000, v186
	v_lshlrev_b32_e32 v186, 16, v187
	v_and_b32_e32 v187, 0xffff0000, v187
	v_max_f32_e32 v180, 0x1e3ce508, v180
	v_max_f32_e32 v181, 0x1e3ce508, v181
	v_max_f32_e32 v182, 0x1e3ce508, v182
	v_max_f32_e32 v183, 0x1e3ce508, v183
	v_max_f32_e32 v184, 0x1e3ce508, v184
	v_max_f32_e32 v185, 0x1e3ce508, v185
	v_max_f32_e32 v186, 0x1e3ce508, v186
	v_max_f32_e32 v187, 0x1e3ce508, v187
	v_rcp_f32_e32 v180, v180
	v_rcp_f32_e32 v181, v181
	v_rcp_f32_e32 v182, v182
	v_rcp_f32_e32 v183, v183
	v_rcp_f32_e32 v184, v184
	v_rcp_f32_e32 v185, v185
	v_rcp_f32_e32 v186, v186
	v_rcp_f32_e32 v187, v187
	v_pk_mul_f32 v[220:221], v[220:221], v[180:181]
	v_pk_mul_f32 v[222:223], v[222:223], v[182:183]
	v_pk_mul_f32 v[224:225], v[224:225], v[184:185]
	v_pk_mul_f32 v[226:227], v[226:227], v[186:187]
	v_pk_mul_f32 v[96:97], v[96:97], v[220:221]
	v_pk_mul_f32 v[98:99], v[98:99], v[222:223]
	v_pk_mul_f32 v[92:93], v[92:93], v[224:225]
	v_pk_mul_f32 v[94:95], v[94:95], v[226:227]
	s_add_u32 s28, s26, 0xd8000
	s_addc_u32 s29, s27, 0
	global_load_dwordx4 v[180:183], v191, s[28:29] offset:256
	global_load_dwordx4 v[184:187], v191, s[28:29] offset:2304
	s_waitcnt vmcnt(11)
	v_lshlrev_b32_e32 v220, 16, v248
	v_and_b32_e32 v221, 0xffff0000, v248
	v_lshlrev_b32_e32 v222, 16, v249
	v_and_b32_e32 v223, 0xffff0000, v249
	v_lshlrev_b32_e32 v224, 16, v250
	v_and_b32_e32 v225, 0xffff0000, v250
	v_lshlrev_b32_e32 v226, 16, v251
	v_and_b32_e32 v227, 0xffff0000, v251
	v_max_f32_e32 v220, 0x1e3ce508, v220
	v_max_f32_e32 v221, 0x1e3ce508, v221
	v_max_f32_e32 v222, 0x1e3ce508, v222
	v_max_f32_e32 v223, 0x1e3ce508, v223
	v_max_f32_e32 v224, 0x1e3ce508, v224
	v_max_f32_e32 v225, 0x1e3ce508, v225
	v_max_f32_e32 v226, 0x1e3ce508, v226
	v_max_f32_e32 v227, 0x1e3ce508, v227
	v_mov_b32_e32 v248, v196
	v_mov_b32_e32 v249, v197
	v_mov_b32_e32 v250, v198
	v_mov_b32_e32 v251, v199
	v_lshlrev_b32_e32 v192, 16, v196
	v_and_b32_e32 v193, 0xffff0000, v196
	v_lshlrev_b32_e32 v194, 16, v197
	v_and_b32_e32 v195, 0xffff0000, v197
	v_lshlrev_b32_e32 v196, 16, v198
	v_and_b32_e32 v197, 0xffff0000, v198
	v_lshlrev_b32_e32 v198, 16, v199
	v_and_b32_e32 v199, 0xffff0000, v199
	v_max_f32_e32 v192, 0x1e3ce508, v192
	v_max_f32_e32 v193, 0x1e3ce508, v193
	v_max_f32_e32 v194, 0x1e3ce508, v194
	v_max_f32_e32 v195, 0x1e3ce508, v195
	v_max_f32_e32 v196, 0x1e3ce508, v196
	v_max_f32_e32 v197, 0x1e3ce508, v197
	v_max_f32_e32 v198, 0x1e3ce508, v198
	v_max_f32_e32 v199, 0x1e3ce508, v199
	v_rcp_f32_e32 v192, v192
	v_rcp_f32_e32 v193, v193
	v_rcp_f32_e32 v194, v194
	v_rcp_f32_e32 v195, v195
	v_rcp_f32_e32 v196, v196
	v_rcp_f32_e32 v197, v197
	v_rcp_f32_e32 v198, v198
	v_rcp_f32_e32 v199, v199
	v_pk_mul_f32 v[220:221], v[220:221], v[192:193]
	v_pk_mul_f32 v[222:223], v[222:223], v[194:195]
	v_pk_mul_f32 v[224:225], v[224:225], v[196:197]
	v_pk_mul_f32 v[226:227], v[226:227], v[198:199]
	v_pk_mul_f32 v[64:65], v[64:65], v[220:221]
	v_pk_mul_f32 v[66:67], v[66:67], v[222:223]
	v_pk_mul_f32 v[60:61], v[60:61], v[224:225]
	v_pk_mul_f32 v[62:63], v[62:63], v[226:227]
	s_add_u32 s28, s26, 0xf0000
	s_addc_u32 s29, s27, 0
	global_load_dwordx4 v[192:195], v191, s[28:29]
	global_load_dwordx4 v[196:199], v191, s[28:29] offset:2048
	s_waitcnt vmcnt(12)
	v_lshlrev_b32_e32 v220, 16, v168
	v_and_b32_e32 v221, 0xffff0000, v168
	v_lshlrev_b32_e32 v222, 16, v169
	v_and_b32_e32 v223, 0xffff0000, v169
	v_lshlrev_b32_e32 v224, 16, v170
	v_and_b32_e32 v225, 0xffff0000, v170
	v_lshlrev_b32_e32 v226, 16, v171
	v_and_b32_e32 v227, 0xffff0000, v171
	v_max_f32_e32 v220, 0x1e3ce508, v220
	v_max_f32_e32 v221, 0x1e3ce508, v221
	v_max_f32_e32 v222, 0x1e3ce508, v222
	v_max_f32_e32 v223, 0x1e3ce508, v223
	v_max_f32_e32 v224, 0x1e3ce508, v224
	v_max_f32_e32 v225, 0x1e3ce508, v225
	v_max_f32_e32 v226, 0x1e3ce508, v226
	v_max_f32_e32 v227, 0x1e3ce508, v227
	v_mov_b32_e32 v168, v216
	v_mov_b32_e32 v169, v217
	v_mov_b32_e32 v170, v218
	v_mov_b32_e32 v171, v219
	v_lshlrev_b32_e32 v212, 16, v216
	v_and_b32_e32 v213, 0xffff0000, v216
	v_lshlrev_b32_e32 v214, 16, v217
	v_and_b32_e32 v215, 0xffff0000, v217
	v_lshlrev_b32_e32 v216, 16, v218
	v_and_b32_e32 v217, 0xffff0000, v218
	v_lshlrev_b32_e32 v218, 16, v219
	v_and_b32_e32 v219, 0xffff0000, v219
	v_max_f32_e32 v212, 0x1e3ce508, v212
	v_max_f32_e32 v213, 0x1e3ce508, v213
	v_max_f32_e32 v214, 0x1e3ce508, v214
	v_max_f32_e32 v215, 0x1e3ce508, v215
	v_max_f32_e32 v216, 0x1e3ce508, v216
	v_max_f32_e32 v217, 0x1e3ce508, v217
	v_max_f32_e32 v218, 0x1e3ce508, v218
	v_max_f32_e32 v219, 0x1e3ce508, v219
	v_rcp_f32_e32 v212, v212
	v_rcp_f32_e32 v213, v213
	v_rcp_f32_e32 v214, v214
	v_rcp_f32_e32 v215, v215
	v_rcp_f32_e32 v216, v216
	v_rcp_f32_e32 v217, v217
	v_rcp_f32_e32 v218, v218
	v_rcp_f32_e32 v219, v219
	v_pk_mul_f32 v[220:221], v[220:221], v[212:213]
	v_pk_mul_f32 v[222:223], v[222:223], v[214:215]
	v_pk_mul_f32 v[224:225], v[224:225], v[216:217]
	v_pk_mul_f32 v[226:227], v[226:227], v[218:219]
	v_pk_mul_f32 v[88:89], v[88:89], v[220:221]
	v_pk_mul_f32 v[90:91], v[90:91], v[222:223]
	v_pk_mul_f32 v[84:85], v[84:85], v[224:225]
	v_pk_mul_f32 v[86:87], v[86:87], v[226:227]
	s_add_u32 s28, s26, 0xf0000
	s_addc_u32 s29, s27, 0
	global_load_dwordx4 v[212:215], v191, s[28:29] offset:256
	global_load_dwordx4 v[216:219], v191, s[28:29] offset:2304
	s_waitcnt vmcnt(12)
	v_lshlrev_b32_e32 v220, 16, v132
	v_and_b32_e32 v221, 0xffff0000, v132
	v_lshlrev_b32_e32 v222, 16, v133
	v_and_b32_e32 v223, 0xffff0000, v133
	v_lshlrev_b32_e32 v224, 16, v134
	v_and_b32_e32 v225, 0xffff0000, v134
	v_lshlrev_b32_e32 v226, 16, v135
	v_and_b32_e32 v227, 0xffff0000, v135
	v_max_f32_e32 v220, 0x1e3ce508, v220
	v_max_f32_e32 v221, 0x1e3ce508, v221
	v_max_f32_e32 v222, 0x1e3ce508, v222
	v_max_f32_e32 v223, 0x1e3ce508, v223
	v_max_f32_e32 v224, 0x1e3ce508, v224
	v_max_f32_e32 v225, 0x1e3ce508, v225
	v_max_f32_e32 v226, 0x1e3ce508, v226
	v_max_f32_e32 v227, 0x1e3ce508, v227
	v_lshlrev_b32_e32 v132, 16, v136
	v_and_b32_e32 v133, 0xffff0000, v136
	v_lshlrev_b32_e32 v134, 16, v137
	v_and_b32_e32 v135, 0xffff0000, v137
	v_lshlrev_b32_e32 v136, 16, v138
	v_and_b32_e32 v137, 0xffff0000, v138
	v_lshlrev_b32_e32 v138, 16, v139
	v_and_b32_e32 v139, 0xffff0000, v139
	v_max_f32_e32 v132, 0x1e3ce508, v132
	v_max_f32_e32 v133, 0x1e3ce508, v133
	v_max_f32_e32 v134, 0x1e3ce508, v134
	v_max_f32_e32 v135, 0x1e3ce508, v135
	v_max_f32_e32 v136, 0x1e3ce508, v136
	v_max_f32_e32 v137, 0x1e3ce508, v137
	v_max_f32_e32 v138, 0x1e3ce508, v138
	v_max_f32_e32 v139, 0x1e3ce508, v139
	v_rcp_f32_e32 v132, v132
	v_rcp_f32_e32 v133, v133
	v_rcp_f32_e32 v134, v134
	v_rcp_f32_e32 v135, v135
	v_rcp_f32_e32 v136, v136
	v_rcp_f32_e32 v137, v137
	v_rcp_f32_e32 v138, v138
	v_rcp_f32_e32 v139, v139
	v_pk_mul_f32 v[220:221], v[220:221], v[132:133]
	v_pk_mul_f32 v[222:223], v[222:223], v[134:135]
	v_pk_mul_f32 v[224:225], v[224:225], v[136:137]
	v_pk_mul_f32 v[226:227], v[226:227], v[138:139]
	v_pk_mul_f32 v[56:57], v[56:57], v[220:221]
	v_pk_mul_f32 v[58:59], v[58:59], v[222:223]
	v_pk_mul_f32 v[48:49], v[48:49], v[224:225]
	v_pk_mul_f32 v[50:51], v[50:51], v[226:227]
	s_add_u32 s28, s26, 0x108000
	s_addc_u32 s29, s27, 0
	global_load_dwordx4 v[132:135], v191, s[28:29]
	global_load_dwordx4 v[136:139], v191, s[28:29] offset:2048
	s_waitcnt vmcnt(12)
	v_lshlrev_b32_e32 v220, 16, v140
	v_and_b32_e32 v221, 0xffff0000, v140
	v_lshlrev_b32_e32 v222, 16, v141
	v_and_b32_e32 v223, 0xffff0000, v141
	v_lshlrev_b32_e32 v224, 16, v142
	v_and_b32_e32 v225, 0xffff0000, v142
	v_lshlrev_b32_e32 v226, 16, v143
	v_and_b32_e32 v227, 0xffff0000, v143
	v_max_f32_e32 v220, 0x1e3ce508, v220
	v_max_f32_e32 v221, 0x1e3ce508, v221
	v_max_f32_e32 v222, 0x1e3ce508, v222
	v_max_f32_e32 v223, 0x1e3ce508, v223
	v_max_f32_e32 v224, 0x1e3ce508, v224
	v_max_f32_e32 v225, 0x1e3ce508, v225
	v_max_f32_e32 v226, 0x1e3ce508, v226
	v_max_f32_e32 v227, 0x1e3ce508, v227
	v_lshlrev_b32_e32 v140, 16, v144
	v_and_b32_e32 v141, 0xffff0000, v144
	v_lshlrev_b32_e32 v142, 16, v145
	v_and_b32_e32 v143, 0xffff0000, v145
	v_lshlrev_b32_e32 v144, 16, v146
	v_and_b32_e32 v145, 0xffff0000, v146
	v_lshlrev_b32_e32 v146, 16, v147
	v_and_b32_e32 v147, 0xffff0000, v147
	v_max_f32_e32 v140, 0x1e3ce508, v140
	v_max_f32_e32 v141, 0x1e3ce508, v141
	v_max_f32_e32 v142, 0x1e3ce508, v142
	v_max_f32_e32 v143, 0x1e3ce508, v143
	v_max_f32_e32 v144, 0x1e3ce508, v144
	v_max_f32_e32 v145, 0x1e3ce508, v145
	v_max_f32_e32 v146, 0x1e3ce508, v146
	v_max_f32_e32 v147, 0x1e3ce508, v147
	v_rcp_f32_e32 v140, v140
	v_rcp_f32_e32 v141, v141
	v_rcp_f32_e32 v142, v142
	v_rcp_f32_e32 v143, v143
	v_rcp_f32_e32 v144, v144
	v_rcp_f32_e32 v145, v145
	v_rcp_f32_e32 v146, v146
	v_rcp_f32_e32 v147, v147
	v_pk_mul_f32 v[220:221], v[220:221], v[140:141]
	v_pk_mul_f32 v[222:223], v[222:223], v[142:143]
	v_pk_mul_f32 v[224:225], v[224:225], v[144:145]
	v_pk_mul_f32 v[226:227], v[226:227], v[146:147]
	v_pk_mul_f32 v[52:53], v[52:53], v[220:221]
	v_pk_mul_f32 v[54:55], v[54:55], v[222:223]
	v_pk_mul_f32 v[44:45], v[44:45], v[224:225]
	v_pk_mul_f32 v[46:47], v[46:47], v[226:227]
	s_add_u32 s28, s26, 0x108000
	s_addc_u32 s29, s27, 0
	global_load_dwordx4 v[140:143], v191, s[28:29] offset:256
	global_load_dwordx4 v[144:147], v191, s[28:29] offset:2304
	s_waitcnt vmcnt(12)
	v_lshlrev_b32_e32 v220, 16, v148
	v_and_b32_e32 v221, 0xffff0000, v148
	v_lshlrev_b32_e32 v222, 16, v149
	v_and_b32_e32 v223, 0xffff0000, v149
	v_lshlrev_b32_e32 v224, 16, v150
	v_and_b32_e32 v225, 0xffff0000, v150
	v_lshlrev_b32_e32 v226, 16, v151
	v_and_b32_e32 v227, 0xffff0000, v151
	v_max_f32_e32 v220, 0x1e3ce508, v220
	v_max_f32_e32 v221, 0x1e3ce508, v221
	v_max_f32_e32 v222, 0x1e3ce508, v222
	v_max_f32_e32 v223, 0x1e3ce508, v223
	v_max_f32_e32 v224, 0x1e3ce508, v224
	v_max_f32_e32 v225, 0x1e3ce508, v225
	v_max_f32_e32 v226, 0x1e3ce508, v226
	v_max_f32_e32 v227, 0x1e3ce508, v227
	v_lshlrev_b32_e32 v148, 16, v152
	v_and_b32_e32 v149, 0xffff0000, v152
	v_lshlrev_b32_e32 v150, 16, v153
	v_and_b32_e32 v151, 0xffff0000, v153
	v_lshlrev_b32_e32 v152, 16, v154
	v_and_b32_e32 v153, 0xffff0000, v154
	v_lshlrev_b32_e32 v154, 16, v155
	v_and_b32_e32 v155, 0xffff0000, v155
	v_max_f32_e32 v148, 0x1e3ce508, v148
	v_max_f32_e32 v149, 0x1e3ce508, v149
	v_max_f32_e32 v150, 0x1e3ce508, v150
	v_max_f32_e32 v151, 0x1e3ce508, v151
	v_max_f32_e32 v152, 0x1e3ce508, v152
	v_max_f32_e32 v153, 0x1e3ce508, v153
	v_max_f32_e32 v154, 0x1e3ce508, v154
	v_max_f32_e32 v155, 0x1e3ce508, v155
	v_rcp_f32_e32 v148, v148
	v_rcp_f32_e32 v149, v149
	v_rcp_f32_e32 v150, v150
	v_rcp_f32_e32 v151, v151
	v_rcp_f32_e32 v152, v152
	v_rcp_f32_e32 v153, v153
	v_rcp_f32_e32 v154, v154
	v_rcp_f32_e32 v155, v155
	v_pk_mul_f32 v[220:221], v[220:221], v[148:149]
	v_pk_mul_f32 v[222:223], v[222:223], v[150:151]
	v_pk_mul_f32 v[224:225], v[224:225], v[152:153]
	v_pk_mul_f32 v[226:227], v[226:227], v[154:155]
	v_pk_mul_f32 v[16:17], v[16:17], v[220:221]
	v_pk_mul_f32 v[18:19], v[18:19], v[222:223]
	v_pk_mul_f32 v[12:13], v[12:13], v[224:225]
	v_pk_mul_f32 v[14:15], v[14:15], v[226:227]
	s_waitcnt vmcnt(10)
	v_lshlrev_b32_e32 v220, 16, v156
	v_and_b32_e32 v221, 0xffff0000, v156
	v_lshlrev_b32_e32 v222, 16, v157
	v_and_b32_e32 v223, 0xffff0000, v157
	v_lshlrev_b32_e32 v224, 16, v158
	v_and_b32_e32 v225, 0xffff0000, v158
	v_lshlrev_b32_e32 v226, 16, v159
	v_and_b32_e32 v227, 0xffff0000, v159
	v_max_f32_e32 v220, 0x1e3ce508, v220
	v_max_f32_e32 v221, 0x1e3ce508, v221
	v_max_f32_e32 v222, 0x1e3ce508, v222
	v_max_f32_e32 v223, 0x1e3ce508, v223
	v_max_f32_e32 v224, 0x1e3ce508, v224
	v_max_f32_e32 v225, 0x1e3ce508, v225
	v_max_f32_e32 v226, 0x1e3ce508, v226
	v_max_f32_e32 v227, 0x1e3ce508, v227
	v_lshlrev_b32_e32 v156, 16, v160
	v_and_b32_e32 v157, 0xffff0000, v160
	v_lshlrev_b32_e32 v158, 16, v161
	v_and_b32_e32 v159, 0xffff0000, v161
	v_lshlrev_b32_e32 v160, 16, v162
	v_and_b32_e32 v161, 0xffff0000, v162
	v_lshlrev_b32_e32 v162, 16, v163
	v_and_b32_e32 v163, 0xffff0000, v163
	v_max_f32_e32 v156, 0x1e3ce508, v156
	v_max_f32_e32 v157, 0x1e3ce508, v157
	v_max_f32_e32 v158, 0x1e3ce508, v158
	v_max_f32_e32 v159, 0x1e3ce508, v159
	v_max_f32_e32 v160, 0x1e3ce508, v160
	v_max_f32_e32 v161, 0x1e3ce508, v161
	v_max_f32_e32 v162, 0x1e3ce508, v162
	v_max_f32_e32 v163, 0x1e3ce508, v163
	v_rcp_f32_e32 v156, v156
	v_rcp_f32_e32 v157, v157
	v_rcp_f32_e32 v158, v158
	v_rcp_f32_e32 v159, v159
	v_rcp_f32_e32 v160, v160
	v_rcp_f32_e32 v161, v161
	v_rcp_f32_e32 v162, v162
	v_rcp_f32_e32 v163, v163
	v_pk_mul_f32 v[220:221], v[220:221], v[156:157]
	v_pk_mul_f32 v[222:223], v[222:223], v[158:159]
	v_pk_mul_f32 v[224:225], v[224:225], v[160:161]
	v_pk_mul_f32 v[226:227], v[226:227], v[162:163]
	v_pk_mul_f32 v[40:41], v[40:41], v[220:221]
	v_pk_mul_f32 v[42:43], v[42:43], v[222:223]
	v_pk_mul_f32 v[36:37], v[36:37], v[224:225]
	v_pk_mul_f32 v[38:39], v[38:39], v[226:227]
	s_waitcnt vmcnt(8)
	v_lshlrev_b32_e32 v220, 16, v180
	v_and_b32_e32 v221, 0xffff0000, v180
	v_lshlrev_b32_e32 v222, 16, v181
	v_and_b32_e32 v223, 0xffff0000, v181
	v_lshlrev_b32_e32 v224, 16, v182
	v_and_b32_e32 v225, 0xffff0000, v182
	v_lshlrev_b32_e32 v226, 16, v183
	v_and_b32_e32 v227, 0xffff0000, v183
	v_max_f32_e32 v220, 0x1e3ce508, v220
	v_max_f32_e32 v221, 0x1e3ce508, v221
	v_max_f32_e32 v222, 0x1e3ce508, v222
	v_max_f32_e32 v223, 0x1e3ce508, v223
	v_max_f32_e32 v224, 0x1e3ce508, v224
	v_max_f32_e32 v225, 0x1e3ce508, v225
	v_max_f32_e32 v226, 0x1e3ce508, v226
	v_max_f32_e32 v227, 0x1e3ce508, v227
	v_lshlrev_b32_e32 v180, 16, v184
	v_and_b32_e32 v181, 0xffff0000, v184
	v_lshlrev_b32_e32 v182, 16, v185
	v_and_b32_e32 v183, 0xffff0000, v185
	v_lshlrev_b32_e32 v184, 16, v186
	v_and_b32_e32 v185, 0xffff0000, v186
	v_lshlrev_b32_e32 v186, 16, v187
	v_and_b32_e32 v187, 0xffff0000, v187
	v_max_f32_e32 v180, 0x1e3ce508, v180
	v_max_f32_e32 v181, 0x1e3ce508, v181
	v_max_f32_e32 v182, 0x1e3ce508, v182
	v_max_f32_e32 v183, 0x1e3ce508, v183
	v_max_f32_e32 v184, 0x1e3ce508, v184
	v_max_f32_e32 v185, 0x1e3ce508, v185
	v_max_f32_e32 v186, 0x1e3ce508, v186
	v_max_f32_e32 v187, 0x1e3ce508, v187
	v_rcp_f32_e32 v180, v180
	v_rcp_f32_e32 v181, v181
	v_rcp_f32_e32 v182, v182
	v_rcp_f32_e32 v183, v183
	v_rcp_f32_e32 v184, v184
	v_rcp_f32_e32 v185, v185
	v_rcp_f32_e32 v186, v186
	v_rcp_f32_e32 v187, v187
	v_pk_mul_f32 v[220:221], v[220:221], v[180:181]
	v_pk_mul_f32 v[222:223], v[222:223], v[182:183]
	v_pk_mul_f32 v[224:225], v[224:225], v[184:185]
	v_pk_mul_f32 v[226:227], v[226:227], v[186:187]
	v_pk_mul_f32 v[8:9], v[8:9], v[220:221]
	v_pk_mul_f32 v[10:11], v[10:11], v[222:223]
	v_pk_mul_f32 v[4:5], v[4:5], v[224:225]
	v_pk_mul_f32 v[6:7], v[6:7], v[226:227]
	s_waitcnt vmcnt(6)
	v_lshlrev_b32_e32 v220, 16, v192
	v_and_b32_e32 v221, 0xffff0000, v192
	v_lshlrev_b32_e32 v222, 16, v193
	v_and_b32_e32 v223, 0xffff0000, v193
	v_lshlrev_b32_e32 v224, 16, v194
	v_and_b32_e32 v225, 0xffff0000, v194
	v_lshlrev_b32_e32 v226, 16, v195
	v_and_b32_e32 v227, 0xffff0000, v195
	v_max_f32_e32 v220, 0x1e3ce508, v220
	v_max_f32_e32 v221, 0x1e3ce508, v221
	v_max_f32_e32 v222, 0x1e3ce508, v222
	v_max_f32_e32 v223, 0x1e3ce508, v223
	v_max_f32_e32 v224, 0x1e3ce508, v224
	v_max_f32_e32 v225, 0x1e3ce508, v225
	v_max_f32_e32 v226, 0x1e3ce508, v226
	v_max_f32_e32 v227, 0x1e3ce508, v227
	v_lshlrev_b32_e32 v192, 16, v196
	v_and_b32_e32 v193, 0xffff0000, v196
	v_lshlrev_b32_e32 v194, 16, v197
	v_and_b32_e32 v195, 0xffff0000, v197
	v_lshlrev_b32_e32 v196, 16, v198
	v_and_b32_e32 v197, 0xffff0000, v198
	v_lshlrev_b32_e32 v198, 16, v199
	v_and_b32_e32 v199, 0xffff0000, v199
	v_max_f32_e32 v192, 0x1e3ce508, v192
	v_max_f32_e32 v193, 0x1e3ce508, v193
	v_max_f32_e32 v194, 0x1e3ce508, v194
	v_max_f32_e32 v195, 0x1e3ce508, v195
	v_max_f32_e32 v196, 0x1e3ce508, v196
	v_max_f32_e32 v197, 0x1e3ce508, v197
	v_max_f32_e32 v198, 0x1e3ce508, v198
	v_max_f32_e32 v199, 0x1e3ce508, v199
	v_rcp_f32_e32 v192, v192
	v_rcp_f32_e32 v193, v193
	v_rcp_f32_e32 v194, v194
	v_rcp_f32_e32 v195, v195
	v_rcp_f32_e32 v196, v196
	v_rcp_f32_e32 v197, v197
	v_rcp_f32_e32 v198, v198
	v_rcp_f32_e32 v199, v199
	v_pk_mul_f32 v[220:221], v[220:221], v[192:193]
	v_pk_mul_f32 v[222:223], v[222:223], v[194:195]
	v_pk_mul_f32 v[224:225], v[224:225], v[196:197]
	v_pk_mul_f32 v[226:227], v[226:227], v[198:199]
	v_pk_mul_f32 v[32:33], v[32:33], v[220:221]
	v_pk_mul_f32 v[34:35], v[34:35], v[222:223]
	v_pk_mul_f32 v[28:29], v[28:29], v[224:225]
	v_pk_mul_f32 v[30:31], v[30:31], v[226:227]
	s_waitcnt vmcnt(4)
	v_lshlrev_b32_e32 v220, 16, v212
	v_and_b32_e32 v221, 0xffff0000, v212
	v_lshlrev_b32_e32 v222, 16, v213
	v_and_b32_e32 v223, 0xffff0000, v213
	v_lshlrev_b32_e32 v224, 16, v214
	v_and_b32_e32 v225, 0xffff0000, v214
	v_lshlrev_b32_e32 v226, 16, v215
	v_and_b32_e32 v227, 0xffff0000, v215
	v_max_f32_e32 v220, 0x1e3ce508, v220
	v_max_f32_e32 v221, 0x1e3ce508, v221
	v_max_f32_e32 v222, 0x1e3ce508, v222
	v_max_f32_e32 v223, 0x1e3ce508, v223
	v_max_f32_e32 v224, 0x1e3ce508, v224
	v_max_f32_e32 v225, 0x1e3ce508, v225
	v_max_f32_e32 v226, 0x1e3ce508, v226
	v_max_f32_e32 v227, 0x1e3ce508, v227
	v_lshlrev_b32_e32 v212, 16, v216
	v_and_b32_e32 v213, 0xffff0000, v216
	v_lshlrev_b32_e32 v214, 16, v217
	v_and_b32_e32 v215, 0xffff0000, v217
	v_lshlrev_b32_e32 v216, 16, v218
	v_and_b32_e32 v217, 0xffff0000, v218
	v_lshlrev_b32_e32 v218, 16, v219
	v_and_b32_e32 v219, 0xffff0000, v219
	v_max_f32_e32 v212, 0x1e3ce508, v212
	v_max_f32_e32 v213, 0x1e3ce508, v213
	v_max_f32_e32 v214, 0x1e3ce508, v214
	v_max_f32_e32 v215, 0x1e3ce508, v215
	v_max_f32_e32 v216, 0x1e3ce508, v216
	v_max_f32_e32 v217, 0x1e3ce508, v217
	v_max_f32_e32 v218, 0x1e3ce508, v218
	v_max_f32_e32 v219, 0x1e3ce508, v219
	v_rcp_f32_e32 v212, v212
	v_rcp_f32_e32 v213, v213
	v_rcp_f32_e32 v214, v214
	v_rcp_f32_e32 v215, v215
	v_rcp_f32_e32 v216, v216
	v_rcp_f32_e32 v217, v217
	v_rcp_f32_e32 v218, v218
	v_rcp_f32_e32 v219, v219
	v_pk_mul_f32 v[220:221], v[220:221], v[212:213]
	v_pk_mul_f32 v[222:223], v[222:223], v[214:215]
	v_pk_mul_f32 v[224:225], v[224:225], v[216:217]
	v_pk_mul_f32 v[226:227], v[226:227], v[218:219]
	v_pk_mul_f32 v[116:117], v[116:117], v[220:221]
	v_pk_mul_f32 v[118:119], v[118:119], v[222:223]
	v_pk_mul_f32 v[120:121], v[120:121], v[224:225]
	v_pk_mul_f32 v[122:123], v[122:123], v[226:227]
	s_waitcnt vmcnt(2)
	v_lshlrev_b32_e32 v220, 16, v132
	v_and_b32_e32 v221, 0xffff0000, v132
	v_lshlrev_b32_e32 v222, 16, v133
	v_and_b32_e32 v223, 0xffff0000, v133
	v_lshlrev_b32_e32 v224, 16, v134
	v_and_b32_e32 v225, 0xffff0000, v134
	v_lshlrev_b32_e32 v226, 16, v135
	v_and_b32_e32 v227, 0xffff0000, v135
	v_max_f32_e32 v220, 0x1e3ce508, v220
	v_max_f32_e32 v221, 0x1e3ce508, v221
	v_max_f32_e32 v222, 0x1e3ce508, v222
	v_max_f32_e32 v223, 0x1e3ce508, v223
	v_max_f32_e32 v224, 0x1e3ce508, v224
	v_max_f32_e32 v225, 0x1e3ce508, v225
	v_max_f32_e32 v226, 0x1e3ce508, v226
	v_max_f32_e32 v227, 0x1e3ce508, v227
	v_lshlrev_b32_e32 v132, 16, v136
	v_and_b32_e32 v133, 0xffff0000, v136
	v_lshlrev_b32_e32 v134, 16, v137
	v_and_b32_e32 v135, 0xffff0000, v137
	v_lshlrev_b32_e32 v136, 16, v138
	v_and_b32_e32 v137, 0xffff0000, v138
	v_lshlrev_b32_e32 v138, 16, v139
	v_and_b32_e32 v139, 0xffff0000, v139
	v_max_f32_e32 v132, 0x1e3ce508, v132
	v_max_f32_e32 v133, 0x1e3ce508, v133
	v_max_f32_e32 v134, 0x1e3ce508, v134
	v_max_f32_e32 v135, 0x1e3ce508, v135
	v_max_f32_e32 v136, 0x1e3ce508, v136
	v_max_f32_e32 v137, 0x1e3ce508, v137
	v_max_f32_e32 v138, 0x1e3ce508, v138
	v_max_f32_e32 v139, 0x1e3ce508, v139
	v_rcp_f32_e32 v132, v132
	v_rcp_f32_e32 v133, v133
	v_rcp_f32_e32 v134, v134
	v_rcp_f32_e32 v135, v135
	v_rcp_f32_e32 v136, v136
	v_rcp_f32_e32 v137, v137
	v_rcp_f32_e32 v138, v138
	v_rcp_f32_e32 v139, v139
	v_pk_mul_f32 v[220:221], v[220:221], v[132:133]
	v_pk_mul_f32 v[222:223], v[222:223], v[134:135]
	v_pk_mul_f32 v[224:225], v[224:225], v[136:137]
	v_pk_mul_f32 v[226:227], v[226:227], v[138:139]
	v_pk_mul_f32 v[24:25], v[24:25], v[220:221]
	v_pk_mul_f32 v[26:27], v[26:27], v[222:223]
	v_pk_mul_f32 v[20:21], v[20:21], v[224:225]
	v_pk_mul_f32 v[22:23], v[22:23], v[226:227]
	s_waitcnt vmcnt(0)
	v_lshlrev_b32_e32 v220, 16, v140
	v_and_b32_e32 v221, 0xffff0000, v140
	v_lshlrev_b32_e32 v222, 16, v141
	v_and_b32_e32 v223, 0xffff0000, v141
	v_lshlrev_b32_e32 v224, 16, v142
	v_and_b32_e32 v225, 0xffff0000, v142
	v_lshlrev_b32_e32 v226, 16, v143
	v_and_b32_e32 v227, 0xffff0000, v143
	v_max_f32_e32 v220, 0x1e3ce508, v220
	v_max_f32_e32 v221, 0x1e3ce508, v221
	v_max_f32_e32 v222, 0x1e3ce508, v222
	v_max_f32_e32 v223, 0x1e3ce508, v223
	v_max_f32_e32 v224, 0x1e3ce508, v224
	v_max_f32_e32 v225, 0x1e3ce508, v225
	v_max_f32_e32 v226, 0x1e3ce508, v226
	v_max_f32_e32 v227, 0x1e3ce508, v227
	v_lshlrev_b32_e32 v140, 16, v144
	v_and_b32_e32 v141, 0xffff0000, v144
	v_lshlrev_b32_e32 v142, 16, v145
	v_and_b32_e32 v143, 0xffff0000, v145
	v_lshlrev_b32_e32 v144, 16, v146
	v_and_b32_e32 v145, 0xffff0000, v146
	v_lshlrev_b32_e32 v146, 16, v147
	v_and_b32_e32 v147, 0xffff0000, v147
	v_max_f32_e32 v140, 0x1e3ce508, v140
	v_max_f32_e32 v141, 0x1e3ce508, v141
	v_max_f32_e32 v142, 0x1e3ce508, v142
	v_max_f32_e32 v143, 0x1e3ce508, v143
	v_max_f32_e32 v144, 0x1e3ce508, v144
	v_max_f32_e32 v145, 0x1e3ce508, v145
	v_max_f32_e32 v146, 0x1e3ce508, v146
	v_max_f32_e32 v147, 0x1e3ce508, v147
	v_rcp_f32_e32 v140, v140
	v_rcp_f32_e32 v141, v141
	v_rcp_f32_e32 v142, v142
	v_rcp_f32_e32 v143, v143
	v_rcp_f32_e32 v144, v144
	v_rcp_f32_e32 v145, v145
	v_rcp_f32_e32 v146, v146
	v_rcp_f32_e32 v147, v147
	v_pk_mul_f32 v[220:221], v[220:221], v[140:141]
	v_pk_mul_f32 v[222:223], v[222:223], v[142:143]
	v_pk_mul_f32 v[224:225], v[224:225], v[144:145]
	v_pk_mul_f32 v[226:227], v[226:227], v[146:147]
	v_pk_mul_f32 v[124:125], v[124:125], v[220:221]
	v_pk_mul_f32 v[126:127], v[126:127], v[222:223]
	v_pk_mul_f32 v[128:129], v[128:129], v[224:225]
	v_pk_mul_f32 v[130:131], v[130:131], v[226:227]
	s_branch .Lmg_done
.Lmg_last:
	s_add_u32 s28, s26, 0x48000
	s_addc_u32 s29, s27, 0
	global_load_dwordx4 v[132:135], v191, s[28:29] offset:256
	s_add_u32 s28, s26, 0xc0000
	s_addc_u32 s29, s27, 0
	global_load_dwordx4 v[136:139], v191, s[28:29]
	s_add_u32 s28, s26, 0xc0000
	s_addc_u32 s29, s27, 0
	global_load_dwordx4 v[140:143], v191, s[28:29] offset:256
	s_add_u32 s28, s26, 0xd8000
	s_addc_u32 s29, s27, 0
	global_load_dwordx4 v[144:147], v191, s[28:29]
	s_add_u32 s28, s26, 0xd8000
	s_addc_u32 s29, s27, 0
	global_load_dwordx4 v[148:151], v191, s[28:29] offset:256
	s_add_u32 s28, s26, 0xf0000
	s_addc_u32 s29, s27, 0
	global_load_dwordx4 v[152:155], v191, s[28:29]
	s_add_u32 s28, s26, 0xf0000
	s_addc_u32 s29, s27, 0
	global_load_dwordx4 v[156:159], v191, s[28:29] offset:256
	s_add_u32 s28, s26, 0x108000
	s_addc_u32 s29, s27, 0
	global_load_dwordx4 v[160:163], v191, s[28:29]
	s_add_u32 s28, s26, 0x108000
	s_addc_u32 s29, s27, 0
	global_load_dwordx4 v[180:183], v191, s[28:29] offset:256
	s_and_b64 vcc, exec, s[20:21]
	s_cbranch_vccz .Lmg_nbb
	s_barrier
.Lmg_nbb:
	v_lshlrev_b32_e32 v220, 16, v228
	v_and_b32_e32 v221, 0xffff0000, v228
	v_lshlrev_b32_e32 v222, 16, v229
	v_and_b32_e32 v223, 0xffff0000, v229
	v_lshlrev_b32_e32 v224, 16, v230
	v_and_b32_e32 v225, 0xffff0000, v230
	v_lshlrev_b32_e32 v226, 16, v231
	v_and_b32_e32 v227, 0xffff0000, v231
	v_max_f32_e32 v220, 0x1e3ce508, v220
	v_max_f32_e32 v221, 0x1e3ce508, v221
	v_max_f32_e32 v222, 0x1e3ce508, v222
	v_max_f32_e32 v223, 0x1e3ce508, v223
	v_max_f32_e32 v224, 0x1e3ce508, v224
	v_max_f32_e32 v225, 0x1e3ce508, v225
	v_max_f32_e32 v226, 0x1e3ce508, v226
	v_max_f32_e32 v227, 0x1e3ce508, v227
	v_pk_mul_f32 v[112:113], v[112:113], v[220:221]
	v_pk_mul_f32 v[114:115], v[114:115], v[222:223]
	v_pk_mul_f32 v[108:109], v[108:109], v[224:225]
	v_pk_mul_f32 v[110:111], v[110:111], v[226:227]
	v_cvt_pk_bf16_f32 v228, v112, v113
	v_cvt_pk_bf16_f32 v229, v114, v115
	v_cvt_pk_bf16_f32 v230, v108, v109
	v_cvt_pk_bf16_f32 v231, v110, v111
	v_lshlrev_b32_e32 v220, 16, v232
	v_and_b32_e32 v221, 0xffff0000, v232
	v_lshlrev_b32_e32 v222, 16, v233
	v_and_b32_e32 v223, 0xffff0000, v233
	v_lshlrev_b32_e32 v224, 16, v234
	v_and_b32_e32 v225, 0xffff0000, v234
	v_lshlrev_b32_e32 v226, 16, v235
	v_and_b32_e32 v227, 0xffff0000, v235
	v_max_f32_e32 v220, 0x1e3ce508, v220
	v_max_f32_e32 v221, 0x1e3ce508, v221
	v_max_f32_e32 v222, 0x1e3ce508, v222
	v_max_f32_e32 v223, 0x1e3ce508, v223
	v_max_f32_e32 v224, 0x1e3ce508, v224
	v_max_f32_e32 v225, 0x1e3ce508, v225
	v_max_f32_e32 v226, 0x1e3ce508, v226
	v_max_f32_e32 v227, 0x1e3ce508, v227
	v_pk_mul_f32 v[80:81], v[80:81], v[220:221]
	v_pk_mul_f32 v[82:83], v[82:83], v[222:223]
	v_pk_mul_f32 v[76:77], v[76:77], v[224:225]
	v_pk_mul_f32 v[78:79], v[78:79], v[226:227]
	v_cvt_pk_bf16_f32 v232, v80, v81
	v_cvt_pk_bf16_f32 v233, v82, v83
	v_cvt_pk_bf16_f32 v234, v76, v77
	v_cvt_pk_bf16_f32 v235, v78, v79
	v_lshlrev_b32_e32 v220, 16, v236
	v_and_b32_e32 v221, 0xffff0000, v236
	v_lshlrev_b32_e32 v222, 16, v237
	v_and_b32_e32 v223, 0xffff0000, v237
	v_lshlrev_b32_e32 v224, 16, v238
	v_and_b32_e32 v225, 0xffff0000, v238
	v_lshlrev_b32_e32 v226, 16, v239
	v_and_b32_e32 v227, 0xffff0000, v239
	v_max_f32_e32 v220, 0x1e3ce508, v220
	v_max_f32_e32 v221, 0x1e3ce508, v221
	v_max_f32_e32 v222, 0x1e3ce508, v222
	v_max_f32_e32 v223, 0x1e3ce508, v223
	v_max_f32_e32 v224, 0x1e3ce508, v224
	v_max_f32_e32 v225, 0x1e3ce508, v225
	v_max_f32_e32 v226, 0x1e3ce508, v226
	v_max_f32_e32 v227, 0x1e3ce508, v227
	v_pk_mul_f32 v[104:105], v[104:105], v[220:221]
	v_pk_mul_f32 v[106:107], v[106:107], v[222:223]
	v_pk_mul_f32 v[100:101], v[100:101], v[224:225]
	v_pk_mul_f32 v[102:103], v[102:103], v[226:227]
	v_cvt_pk_bf16_f32 v236, v104, v105
	v_cvt_pk_bf16_f32 v237, v106, v107
	v_cvt_pk_bf16_f32 v238, v100, v101
	v_cvt_pk_bf16_f32 v239, v102, v103
	v_lshlrev_b32_e32 v220, 16, v240
	v_and_b32_e32 v221, 0xffff0000, v240
	v_lshlrev_b32_e32 v222, 16, v241
	v_and_b32_e32 v223, 0xffff0000, v241
	v_lshlrev_b32_e32 v224, 16, v242
	v_and_b32_e32 v225, 0xffff0000, v242
	v_lshlrev_b32_e32 v226, 16, v243
	v_and_b32_e32 v227, 0xffff0000, v243
	v_max_f32_e32 v220, 0x1e3ce508, v220
	v_max_f32_e32 v221, 0x1e3ce508, v221
	v_max_f32_e32 v222, 0x1e3ce508, v222
	v_max_f32_e32 v223, 0x1e3ce508, v223
	v_max_f32_e32 v224, 0x1e3ce508, v224
	v_max_f32_e32 v225, 0x1e3ce508, v225
	v_max_f32_e32 v226, 0x1e3ce508, v226
	v_max_f32_e32 v227, 0x1e3ce508, v227
	v_pk_mul_f32 v[72:73], v[72:73], v[220:221]
	v_pk_mul_f32 v[74:75], v[74:75], v[222:223]
	v_pk_mul_f32 v[68:69], v[68:69], v[224:225]
	v_pk_mul_f32 v[70:71], v[70:71], v[226:227]
	v_cvt_pk_bf16_f32 v240, v72, v73
	v_cvt_pk_bf16_f32 v241, v74, v75
	v_cvt_pk_bf16_f32 v242, v68, v69
	v_cvt_pk_bf16_f32 v243, v70, v71
	v_lshlrev_b32_e32 v220, 16, v244
	v_and_b32_e32 v221, 0xffff0000, v244
	v_lshlrev_b32_e32 v222, 16, v245
	v_and_b32_e32 v223, 0xffff0000, v245
	v_lshlrev_b32_e32 v224, 16, v246
	v_and_b32_e32 v225, 0xffff0000, v246
	v_lshlrev_b32_e32 v226, 16, v247
	v_and_b32_e32 v227, 0xffff0000, v247
	v_max_f32_e32 v220, 0x1e3ce508, v220
	v_max_f32_e32 v221, 0x1e3ce508, v221
	v_max_f32_e32 v222, 0x1e3ce508, v222
	v_max_f32_e32 v223, 0x1e3ce508, v223
	v_max_f32_e32 v224, 0x1e3ce508, v224
	v_max_f32_e32 v225, 0x1e3ce508, v225
	v_max_f32_e32 v226, 0x1e3ce508, v226
	v_max_f32_e32 v227, 0x1e3ce508, v227
	v_pk_mul_f32 v[96:97], v[96:97], v[220:221]
	v_pk_mul_f32 v[98:99], v[98:99], v[222:223]
	v_pk_mul_f32 v[92:93], v[92:93], v[224:225]
	v_pk_mul_f32 v[94:95], v[94:95], v[226:227]
	v_cvt_pk_bf16_f32 v244, v96, v97
	v_cvt_pk_bf16_f32 v245, v98, v99
	v_cvt_pk_bf16_f32 v246, v92, v93
	v_cvt_pk_bf16_f32 v247, v94, v95
	v_lshlrev_b32_e32 v220, 16, v248
	v_and_b32_e32 v221, 0xffff0000, v248
	v_lshlrev_b32_e32 v222, 16, v249
	v_and_b32_e32 v223, 0xffff0000, v249
	v_lshlrev_b32_e32 v224, 16, v250
	v_and_b32_e32 v225, 0xffff0000, v250
	v_lshlrev_b32_e32 v226, 16, v251
	v_and_b32_e32 v227, 0xffff0000, v251
	v_max_f32_e32 v220, 0x1e3ce508, v220
	v_max_f32_e32 v221, 0x1e3ce508, v221
	v_max_f32_e32 v222, 0x1e3ce508, v222
	v_max_f32_e32 v223, 0x1e3ce508, v223
	v_max_f32_e32 v224, 0x1e3ce508, v224
	v_max_f32_e32 v225, 0x1e3ce508, v225
	v_max_f32_e32 v226, 0x1e3ce508, v226
	v_max_f32_e32 v227, 0x1e3ce508, v227
	v_pk_mul_f32 v[64:65], v[64:65], v[220:221]
	v_pk_mul_f32 v[66:67], v[66:67], v[222:223]
	v_pk_mul_f32 v[60:61], v[60:61], v[224:225]
	v_pk_mul_f32 v[62:63], v[62:63], v[226:227]
	v_cvt_pk_bf16_f32 v248, v64, v65
	v_cvt_pk_bf16_f32 v249, v66, v67
	v_cvt_pk_bf16_f32 v250, v60, v61
	v_cvt_pk_bf16_f32 v251, v62, v63
	v_lshlrev_b32_e32 v220, 16, v168
	v_and_b32_e32 v221, 0xffff0000, v168
	v_lshlrev_b32_e32 v222, 16, v169
	v_and_b32_e32 v223, 0xffff0000, v169
	v_lshlrev_b32_e32 v224, 16, v170
	v_and_b32_e32 v225, 0xffff0000, v170
	v_lshlrev_b32_e32 v226, 16, v171
	v_and_b32_e32 v227, 0xffff0000, v171
	v_max_f32_e32 v220, 0x1e3ce508, v220
	v_max_f32_e32 v221, 0x1e3ce508, v221
	v_max_f32_e32 v222, 0x1e3ce508, v222
	v_max_f32_e32 v223, 0x1e3ce508, v223
	v_max_f32_e32 v224, 0x1e3ce508, v224
	v_max_f32_e32 v225, 0x1e3ce508, v225
	v_max_f32_e32 v226, 0x1e3ce508, v226
	v_max_f32_e32 v227, 0x1e3ce508, v227
	v_pk_mul_f32 v[88:89], v[88:89], v[220:221]
	v_pk_mul_f32 v[90:91], v[90:91], v[222:223]
	v_pk_mul_f32 v[84:85], v[84:85], v[224:225]
	v_pk_mul_f32 v[86:87], v[86:87], v[226:227]
	v_cvt_pk_bf16_f32 v168, v88, v89
	v_cvt_pk_bf16_f32 v169, v90, v91
	v_cvt_pk_bf16_f32 v170, v84, v85
	v_cvt_pk_bf16_f32 v171, v86, v87
	s_waitcnt vmcnt(8)
	v_lshlrev_b32_e32 v220, 16, v132
	v_and_b32_e32 v221, 0xffff0000, v132
	v_lshlrev_b32_e32 v222, 16, v133
	v_and_b32_e32 v223, 0xffff0000, v133
	v_lshlrev_b32_e32 v224, 16, v134
	v_and_b32_e32 v225, 0xffff0000, v134
	v_lshlrev_b32_e32 v226, 16, v135
	v_and_b32_e32 v227, 0xffff0000, v135
	v_max_f32_e32 v220, 0x1e3ce508, v220
	v_max_f32_e32 v221, 0x1e3ce508, v221
	v_max_f32_e32 v222, 0x1e3ce508, v222
	v_max_f32_e32 v223, 0x1e3ce508, v223
	v_max_f32_e32 v224, 0x1e3ce508, v224
	v_max_f32_e32 v225, 0x1e3ce508, v225
	v_max_f32_e32 v226, 0x1e3ce508, v226
	v_max_f32_e32 v227, 0x1e3ce508, v227
	v_pk_mul_f32 v[56:57], v[56:57], v[220:221]
	v_pk_mul_f32 v[58:59], v[58:59], v[222:223]
	v_pk_mul_f32 v[48:49], v[48:49], v[224:225]
	v_pk_mul_f32 v[50:51], v[50:51], v[226:227]
	v_cvt_pk_bf16_f32 v132, v56, v57
	v_cvt_pk_bf16_f32 v133, v58, v59
	v_cvt_pk_bf16_f32 v134, v48, v49
	v_cvt_pk_bf16_f32 v135, v50, v51
	s_waitcnt vmcnt(7)
	v_lshlrev_b32_e32 v220, 16, v136
	v_and_b32_e32 v221, 0xffff0000, v136
	v_lshlrev_b32_e32 v222, 16, v137
	v_and_b32_e32 v223, 0xffff0000, v137
	v_lshlrev_b32_e32 v224, 16, v138
	v_and_b32_e32 v225, 0xffff0000, v138
	v_lshlrev_b32_e32 v226, 16, v139
	v_and_b32_e32 v227, 0xffff0000, v139
	v_max_f32_e32 v220, 0x1e3ce508, v220
	v_max_f32_e32 v221, 0x1e3ce508, v221
	v_max_f32_e32 v222, 0x1e3ce508, v222
	v_max_f32_e32 v223, 0x1e3ce508, v223
	v_max_f32_e32 v224, 0x1e3ce508, v224
	v_max_f32_e32 v225, 0x1e3ce508, v225
	v_max_f32_e32 v226, 0x1e3ce508, v226
	v_max_f32_e32 v227, 0x1e3ce508, v227
	v_pk_mul_f32 v[52:53], v[52:53], v[220:221]
	v_pk_mul_f32 v[54:55], v[54:55], v[222:223]
	v_pk_mul_f32 v[44:45], v[44:45], v[224:225]
	v_pk_mul_f32 v[46:47], v[46:47], v[226:227]
	v_cvt_pk_bf16_f32 v136, v52, v53
	v_cvt_pk_bf16_f32 v137, v54, v55
	v_cvt_pk_bf16_f32 v138, v44, v45
	v_cvt_pk_bf16_f32 v139, v46, v47
	s_waitcnt vmcnt(6)
	v_lshlrev_b32_e32 v220, 16, v140
	v_and_b32_e32 v221, 0xffff0000, v140
	v_lshlrev_b32_e32 v222, 16, v141
	v_and_b32_e32 v223, 0xffff0000, v141
	v_lshlrev_b32_e32 v224, 16, v142
	v_and_b32_e32 v225, 0xffff0000, v142
	v_lshlrev_b32_e32 v226, 16, v143
	v_and_b32_e32 v227, 0xffff0000, v143
	v_max_f32_e32 v220, 0x1e3ce508, v220
	v_max_f32_e32 v221, 0x1e3ce508, v221
	v_max_f32_e32 v222, 0x1e3ce508, v222
	v_max_f32_e32 v223, 0x1e3ce508, v223
	v_max_f32_e32 v224, 0x1e3ce508, v224
	v_max_f32_e32 v225, 0x1e3ce508, v225
	v_max_f32_e32 v226, 0x1e3ce508, v226
	v_max_f32_e32 v227, 0x1e3ce508, v227
	v_pk_mul_f32 v[16:17], v[16:17], v[220:221]
	v_pk_mul_f32 v[18:19], v[18:19], v[222:223]
	v_pk_mul_f32 v[12:13], v[12:13], v[224:225]
	v_pk_mul_f32 v[14:15], v[14:15], v[226:227]
	v_cvt_pk_bf16_f32 v140, v16, v17
	v_cvt_pk_bf16_f32 v141, v18, v19
	v_cvt_pk_bf16_f32 v142, v12, v13
	v_cvt_pk_bf16_f32 v143, v14, v15
	s_waitcnt vmcnt(5)
	v_lshlrev_b32_e32 v220, 16, v144
	v_and_b32_e32 v221, 0xffff0000, v144
	v_lshlrev_b32_e32 v222, 16, v145
	v_and_b32_e32 v223, 0xffff0000, v145
	v_lshlrev_b32_e32 v224, 16, v146
	v_and_b32_e32 v225, 0xffff0000, v146
	v_lshlrev_b32_e32 v226, 16, v147
	v_and_b32_e32 v227, 0xffff0000, v147
	v_max_f32_e32 v220, 0x1e3ce508, v220
	v_max_f32_e32 v221, 0x1e3ce508, v221
	v_max_f32_e32 v222, 0x1e3ce508, v222
	v_max_f32_e32 v223, 0x1e3ce508, v223
	v_max_f32_e32 v224, 0x1e3ce508, v224
	v_max_f32_e32 v225, 0x1e3ce508, v225
	v_max_f32_e32 v226, 0x1e3ce508, v226
	v_max_f32_e32 v227, 0x1e3ce508, v227
	v_pk_mul_f32 v[40:41], v[40:41], v[220:221]
	v_pk_mul_f32 v[42:43], v[42:43], v[222:223]
	v_pk_mul_f32 v[36:37], v[36:37], v[224:225]
	v_pk_mul_f32 v[38:39], v[38:39], v[226:227]
	v_cvt_pk_bf16_f32 v144, v40, v41
	v_cvt_pk_bf16_f32 v145, v42, v43
	v_cvt_pk_bf16_f32 v146, v36, v37
	v_cvt_pk_bf16_f32 v147, v38, v39
	s_waitcnt vmcnt(4)
	v_lshlrev_b32_e32 v220, 16, v148
	v_and_b32_e32 v221, 0xffff0000, v148
	v_lshlrev_b32_e32 v222, 16, v149
	v_and_b32_e32 v223, 0xffff0000, v149
	v_lshlrev_b32_e32 v224, 16, v150
	v_and_b32_e32 v225, 0xffff0000, v150
	v_lshlrev_b32_e32 v226, 16, v151
	v_and_b32_e32 v227, 0xffff0000, v151
	v_max_f32_e32 v220, 0x1e3ce508, v220
	v_max_f32_e32 v221, 0x1e3ce508, v221
	v_max_f32_e32 v222, 0x1e3ce508, v222
	v_max_f32_e32 v223, 0x1e3ce508, v223
	v_max_f32_e32 v224, 0x1e3ce508, v224
	v_max_f32_e32 v225, 0x1e3ce508, v225
	v_max_f32_e32 v226, 0x1e3ce508, v226
	v_max_f32_e32 v227, 0x1e3ce508, v227
	v_pk_mul_f32 v[8:9], v[8:9], v[220:221]
	v_pk_mul_f32 v[10:11], v[10:11], v[222:223]
	v_pk_mul_f32 v[4:5], v[4:5], v[224:225]
	v_pk_mul_f32 v[6:7], v[6:7], v[226:227]
	v_cvt_pk_bf16_f32 v148, v8, v9
	v_cvt_pk_bf16_f32 v149, v10, v11
	v_cvt_pk_bf16_f32 v150, v4, v5
	v_cvt_pk_bf16_f32 v151, v6, v7
	s_waitcnt vmcnt(3)
	v_lshlrev_b32_e32 v220, 16, v152
	v_and_b32_e32 v221, 0xffff0000, v152
	v_lshlrev_b32_e32 v222, 16, v153
	v_and_b32_e32 v223, 0xffff0000, v153
	v_lshlrev_b32_e32 v224, 16, v154
	v_and_b32_e32 v225, 0xffff0000, v154
	v_lshlrev_b32_e32 v226, 16, v155
	v_and_b32_e32 v227, 0xffff0000, v155
	v_max_f32_e32 v220, 0x1e3ce508, v220
	v_max_f32_e32 v221, 0x1e3ce508, v221
	v_max_f32_e32 v222, 0x1e3ce508, v222
	v_max_f32_e32 v223, 0x1e3ce508, v223
	v_max_f32_e32 v224, 0x1e3ce508, v224
	v_max_f32_e32 v225, 0x1e3ce508, v225
	v_max_f32_e32 v226, 0x1e3ce508, v226
	v_max_f32_e32 v227, 0x1e3ce508, v227
	v_pk_mul_f32 v[32:33], v[32:33], v[220:221]
	v_pk_mul_f32 v[34:35], v[34:35], v[222:223]
	v_pk_mul_f32 v[28:29], v[28:29], v[224:225]
	v_pk_mul_f32 v[30:31], v[30:31], v[226:227]
	v_cvt_pk_bf16_f32 v152, v32, v33
	v_cvt_pk_bf16_f32 v153, v34, v35
	v_cvt_pk_bf16_f32 v154, v28, v29
	v_cvt_pk_bf16_f32 v155, v30, v31
	s_waitcnt vmcnt(2)
	v_lshlrev_b32_e32 v220, 16, v156
	v_and_b32_e32 v221, 0xffff0000, v156
	v_lshlrev_b32_e32 v222, 16, v157
	v_and_b32_e32 v223, 0xffff0000, v157
	v_lshlrev_b32_e32 v224, 16, v158
	v_and_b32_e32 v225, 0xffff0000, v158
	v_lshlrev_b32_e32 v226, 16, v159
	v_and_b32_e32 v227, 0xffff0000, v159
	v_max_f32_e32 v220, 0x1e3ce508, v220
	v_max_f32_e32 v221, 0x1e3ce508, v221
	v_max_f32_e32 v222, 0x1e3ce508, v222
	v_max_f32_e32 v223, 0x1e3ce508, v223
	v_max_f32_e32 v224, 0x1e3ce508, v224
	v_max_f32_e32 v225, 0x1e3ce508, v225
	v_max_f32_e32 v226, 0x1e3ce508, v226
	v_max_f32_e32 v227, 0x1e3ce508, v227
	v_pk_mul_f32 v[116:117], v[116:117], v[220:221]
	v_pk_mul_f32 v[118:119], v[118:119], v[222:223]
	v_pk_mul_f32 v[120:121], v[120:121], v[224:225]
	v_pk_mul_f32 v[122:123], v[122:123], v[226:227]
	v_cvt_pk_bf16_f32 v156, v116, v117
	v_cvt_pk_bf16_f32 v157, v118, v119
	v_cvt_pk_bf16_f32 v158, v120, v121
	v_cvt_pk_bf16_f32 v159, v122, v123
	s_waitcnt vmcnt(1)
	v_lshlrev_b32_e32 v220, 16, v160
	v_and_b32_e32 v221, 0xffff0000, v160
	v_lshlrev_b32_e32 v222, 16, v161
	v_and_b32_e32 v223, 0xffff0000, v161
	v_lshlrev_b32_e32 v224, 16, v162
	v_and_b32_e32 v225, 0xffff0000, v162
	v_lshlrev_b32_e32 v226, 16, v163
	v_and_b32_e32 v227, 0xffff0000, v163
	v_max_f32_e32 v220, 0x1e3ce508, v220
	v_max_f32_e32 v221, 0x1e3ce508, v221
	v_max_f32_e32 v222, 0x1e3ce508, v222
	v_max_f32_e32 v223, 0x1e3ce508, v223
	v_max_f32_e32 v224, 0x1e3ce508, v224
	v_max_f32_e32 v225, 0x1e3ce508, v225
	v_max_f32_e32 v226, 0x1e3ce508, v226
	v_max_f32_e32 v227, 0x1e3ce508, v227
	v_pk_mul_f32 v[24:25], v[24:25], v[220:221]
	v_pk_mul_f32 v[26:27], v[26:27], v[222:223]
	v_pk_mul_f32 v[20:21], v[20:21], v[224:225]
	v_pk_mul_f32 v[22:23], v[22:23], v[226:227]
	v_cvt_pk_bf16_f32 v160, v24, v25
	v_cvt_pk_bf16_f32 v161, v26, v27
	v_cvt_pk_bf16_f32 v162, v20, v21
	v_cvt_pk_bf16_f32 v163, v22, v23
	s_waitcnt vmcnt(0)
	v_lshlrev_b32_e32 v220, 16, v180
	v_and_b32_e32 v221, 0xffff0000, v180
	v_lshlrev_b32_e32 v222, 16, v181
	v_and_b32_e32 v223, 0xffff0000, v181
	v_lshlrev_b32_e32 v224, 16, v182
	v_and_b32_e32 v225, 0xffff0000, v182
	v_lshlrev_b32_e32 v226, 16, v183
	v_and_b32_e32 v227, 0xffff0000, v183
	v_max_f32_e32 v220, 0x1e3ce508, v220
	v_max_f32_e32 v221, 0x1e3ce508, v221
	v_max_f32_e32 v222, 0x1e3ce508, v222
	v_max_f32_e32 v223, 0x1e3ce508, v223
	v_max_f32_e32 v224, 0x1e3ce508, v224
	v_max_f32_e32 v225, 0x1e3ce508, v225
	v_max_f32_e32 v226, 0x1e3ce508, v226
	v_max_f32_e32 v227, 0x1e3ce508, v227
	v_pk_mul_f32 v[124:125], v[124:125], v[220:221]
	v_pk_mul_f32 v[126:127], v[126:127], v[222:223]
	v_pk_mul_f32 v[128:129], v[128:129], v[224:225]
	v_pk_mul_f32 v[130:131], v[130:131], v[226:227]
	v_cvt_pk_bf16_f32 v180, v124, v125
	v_cvt_pk_bf16_f32 v181, v126, v127
	v_cvt_pk_bf16_f32 v182, v128, v129
	v_cvt_pk_bf16_f32 v183, v130, v131
	s_add_u32 s6, s16, 0x0
	s_addc_u32 s7, s17, 0
	global_store_dwordx4 v3, v[228:231], s[6:7]
	s_add_u32 s6, s16, 0x0
	s_addc_u32 s7, s17, 0
	global_store_dwordx4 v3, v[232:235], s[6:7] offset:256
	s_add_u32 s6, s16, 0x8000
	s_addc_u32 s7, s17, 0
	global_store_dwordx4 v3, v[236:239], s[6:7]
	s_add_u32 s6, s16, 0x8000
	s_addc_u32 s7, s17, 0
	global_store_dwordx4 v3, v[240:243], s[6:7] offset:256
	s_add_u32 s6, s16, 0x10000
	s_addc_u32 s7, s17, 0
	global_store_dwordx4 v3, v[244:247], s[6:7]
	s_add_u32 s6, s16, 0x10000
	s_addc_u32 s7, s17, 0
	global_store_dwordx4 v3, v[248:251], s[6:7] offset:256
	s_add_u32 s6, s16, 0x18000
	s_addc_u32 s7, s17, 0
	global_store_dwordx4 v3, v[168:171], s[6:7]
	s_add_u32 s6, s16, 0x18000
	s_addc_u32 s7, s17, 0
	global_store_dwordx4 v3, v[132:135], s[6:7] offset:256
	s_add_u32 s6, s16, 0x40000
	s_addc_u32 s7, s17, 0
	global_store_dwordx4 v3, v[136:139], s[6:7]
	s_add_u32 s6, s16, 0x40000
	s_addc_u32 s7, s17, 0
	global_store_dwordx4 v3, v[140:143], s[6:7] offset:256
	s_add_u32 s6, s16, 0x48000
	s_addc_u32 s7, s17, 0
	global_store_dwordx4 v3, v[144:147], s[6:7]
	s_add_u32 s6, s16, 0x48000
	s_addc_u32 s7, s17, 0
	global_store_dwordx4 v3, v[148:151], s[6:7] offset:256
	s_add_u32 s6, s16, 0x50000
	s_addc_u32 s7, s17, 0
	global_store_dwordx4 v3, v[152:155], s[6:7]
	s_add_u32 s6, s16, 0x50000
	s_addc_u32 s7, s17, 0
	global_store_dwordx4 v3, v[156:159], s[6:7] offset:256
	s_add_u32 s6, s16, 0x58000
	s_addc_u32 s7, s17, 0
	global_store_dwordx4 v3, v[160:163], s[6:7]
	s_add_u32 s6, s16, 0x58000
	s_addc_u32 s7, s17, 0
	global_store_dwordx4 v3, v[180:183], s[6:7] offset:256
